# merge epilogues: all gate loads (g and h, 32 per segment) prefetched 8 rounds ahead with counted vmcnt (1)
# baseline (speedup 1.0000x reference)
; __device__ __forceinline__ u32x4 pack8(f32x4 v0, f32x4 v1) { u32x4 w; w.x = cvt_pk_bf16(v0[0], v0[1]); w.y = cvt_pk_bf16(v0[2], v0[3]); w.z = cvt_pk_bf16(v1[0], v1[1]); w.w = cvt_pk_bf16(v1[2], v1[3]); return w; }
; template <class T> __device__ __forceinline__ void est(T* p, T v) { if constexpr (MK_EPI_NT != 0) __builtin_nontemporal_store(v, p); else *p = v; }
;     __device__ __forceinline__ bool operator()(f32x4 (&acc)[2][2][4][2], const Unit& u, int wr, int wc, int fr, int fq) const {
;         const int row0 = u.pm * 256 + wr * 64 + fr, col0 = u.pn * 256 + wc * 32 + 8 * fq;
;         const int gc = u.z == 0 ? 0 : (u.z == 1 ? 2 : 1), gn = u.z == 0 ? 2 : 1;
; #pragma unroll
;         for (int ai = 0; ai < 2; ++ai)
; #pragma unroll
;             for (int m = 0; m < 4; ++m) { const int row = row0 + ai * 128 + m * 16;
; #pragma unroll
;                 for (int bj = 0; bj < 2; ++bj) { const int col = col0 + bj * 128; f32x4 g0, g1; unpack8_u8(*(const u32x2*)(G8 + (size_t)row * (NIN - C_G) + gc * DM + col), g0, g1);
;                     if (u.z < 2) { f32x4 h0, h1; unpack8_u8(*(const u32x2*)(G8 + (size_t)row * (NIN - C_G) + gn * DM + col), h0, h1);
; #pragma unroll
;                         for (int j = 0; j < 4; ++j) { g0[j] *= __builtin_amdgcn_rcpf(h0[j]); g1[j] *= __builtin_amdgcn_rcpf(h1[j]); }
;                         acc[ai][bj][m][0] *= g0; acc[ai][bj][m][1] *= g1;
;                     } else est((u32x4*)(mrgb + (size_t)row * DM + col), (u32x4)pack8(acc[ai][bj][m][0] * (g0 * (1.f / 255.f)), acc[ai][bj][m][1] * (g1 * (1.f / 255.f)))); } }
;         return u.z < 2;
.LBB0_839:
	s_cmp_eq_u32 s37, 1
	s_cselect_b32 s0, s87, 0x800
	s_cmp_eq_u32 s37, 0
	v_lshl_add_u32 v146, s38, 8, v162
	v_mov_b64_e32 v[148:149], s[64:65]
	v_lshl_or_b32 v4, s8, 8, v164
	s_cselect_b32 s8, 0, s0
	v_mad_i64_i32 v[152:153], s[0:1], v146, s88, v[148:149]
	v_lshl_add_u64 v[148:149], v[152:153], 0, s[8:9]
	v_ashrrev_i32_e32 v5, 31, v4
	v_lshl_add_u64 v[150:151], v[148:149], 0, v[4:5]
	v_mov_b64_e32 v[208:209], v[150:151]
	s_movk_i32 s100, 0x800
	s_cmp_eq_u32 s37, 0
	s_cselect_b32 s100, 0x1000, s100
	s_mov_b32 s101, 0
	v_lshl_add_u64 v[210:211], v[152:153], 0, s[100:101]
	v_lshl_add_u64 v[210:211], v[210:211], 0, v[4:5]
	global_load_dwordx2 v[174:175], v[208:209], off
	global_load_dwordx2 v[190:191], v[210:211], off
	global_load_dwordx2 v[176:177], v[208:209], off offset:128
	global_load_dwordx2 v[192:193], v[210:211], off offset:128
	s_mov_b32 s100, 0x18000
	v_lshl_add_u64 v[212:213], v[208:209], 0, s[100:101]
	global_load_dwordx2 v[178:179], v[212:213], off
	s_mov_b32 s100, 0x18000
	v_lshl_add_u64 v[214:215], v[210:211], 0, s[100:101]
	global_load_dwordx2 v[196:197], v[214:215], off
	s_mov_b32 s100, 0x18000
	v_lshl_add_u64 v[212:213], v[208:209], 0, s[100:101]
	global_load_dwordx2 v[180:181], v[212:213], off offset:128
	s_mov_b32 s100, 0x18000
	v_lshl_add_u64 v[214:215], v[210:211], 0, s[100:101]
	global_load_dwordx2 v[198:199], v[214:215], off offset:128
	s_mov_b32 s100, 0x30000
	v_lshl_add_u64 v[212:213], v[208:209], 0, s[100:101]
	global_load_dwordx2 v[182:183], v[212:213], off
	s_mov_b32 s100, 0x30000
	v_lshl_add_u64 v[214:215], v[210:211], 0, s[100:101]
	global_load_dwordx2 v[200:201], v[214:215], off
	s_mov_b32 s100, 0x30000
	v_lshl_add_u64 v[212:213], v[208:209], 0, s[100:101]
	global_load_dwordx2 v[184:185], v[212:213], off offset:128
	s_mov_b32 s100, 0x30000
	v_lshl_add_u64 v[214:215], v[210:211], 0, s[100:101]
	global_load_dwordx2 v[202:203], v[214:215], off offset:128
	s_mov_b32 s100, 0x48000
	v_lshl_add_u64 v[212:213], v[208:209], 0, s[100:101]
	global_load_dwordx2 v[186:187], v[212:213], off
	s_mov_b32 s100, 0x48000
	v_lshl_add_u64 v[214:215], v[210:211], 0, s[100:101]
	global_load_dwordx2 v[204:205], v[214:215], off
	s_mov_b32 s100, 0x48000
	v_lshl_add_u64 v[212:213], v[208:209], 0, s[100:101]
	global_load_dwordx2 v[188:189], v[212:213], off offset:128
	s_mov_b32 s100, 0x48000
	v_lshl_add_u64 v[214:215], v[210:211], 0, s[100:101]
	global_load_dwordx2 v[206:207], v[214:215], off offset:128
	v_ashrrev_i32_e32 v147, 31, v146
	s_cselect_b32 s82, s87, 0x800
	v_lshlrev_b64 v[148:149], 12, v[146:147]
	s_cmp_gt_i32 s37, 1
	s_cselect_b64 s[84:85], -1, 0
	v_lshl_add_u64 v[148:149], s[60:61], 0, v[148:149]
	s_mov_b64 s[0:1], -1
	s_and_b64 vcc, exec, s[84:85]
	v_lshl_add_u64 v[148:149], v[4:5], 1, v[148:149]
	s_waitcnt vmcnt(15)
	v_mov_b32_e32 v166, v174
	v_mov_b32_e32 v167, v175
	s_mov_b32 s100, 0xc0000
	v_lshl_add_u64 v[212:213], v[208:209], 0, s[100:101]
	global_load_dwordx2 v[174:175], v[212:213], off
	v_cvt_f32_ubyte1_e32 v157, v166
	v_cvt_f32_ubyte0_e32 v156, v166
	v_cvt_f32_ubyte3_e32 v161, v166
	v_cvt_f32_ubyte2_e32 v160, v166
	v_cvt_f32_ubyte1_e32 v155, v167
	v_cvt_f32_ubyte0_e32 v154, v167
	v_cvt_f32_ubyte3_e32 v159, v167
	v_cvt_f32_ubyte2_e32 v158, v167
	s_cbranch_vccz .LBB0_841
	v_pk_mul_f32 v[166:167], v[156:157], s[30:31] op_sel_hi:[1,0]
	v_pk_mul_f32 v[168:169], v[160:161], s[30:31] op_sel_hi:[1,0]
	v_pk_mul_f32 v[166:167], v[130:131], v[166:167]
	v_pk_mul_f32 v[168:169], v[132:133], v[168:169]
	v_pk_mul_f32 v[170:171], v[154:155], s[30:31] op_sel_hi:[1,0]
	v_pk_mul_f32 v[172:173], v[158:159], s[30:31] op_sel_hi:[1,0]
	v_pk_mul_f32 v[170:171], v[126:127], v[170:171]
	v_pk_mul_f32 v[172:173], v[128:129], v[172:173]
	v_cvt_pk_bf16_f32 v166, v166, v167
	v_cvt_pk_bf16_f32 v167, v168, v169
	v_cvt_pk_bf16_f32 v168, v170, v171
	s_mov_b64 s[0:1], 0
	v_cvt_pk_bf16_f32 v169, v172, v173
	global_store_dwordx4 v[148:149], v[166:169], off
.LBB0_841:
	s_mov_b32 s83, s9
	v_lshl_add_u64 v[152:153], v[152:153], 0, s[82:83]
	s_andn2_b64 vcc, exec, s[0:1]
	v_lshl_add_u64 v[152:153], v[152:153], 0, v[4:5]
	s_cbranch_vccnz .LBB0_843
	s_nop 0
	s_waitcnt vmcnt(15)
	v_mov_b32_e32 v166, v190
	v_mov_b32_e32 v167, v191
	v_cvt_f32_ubyte0_e32 v3, v166
	v_cvt_f32_ubyte1_e32 v147, v166
	v_cvt_f32_ubyte2_e32 v170, v166
	v_cvt_f32_ubyte3_e32 v171, v166
	v_cvt_f32_ubyte0_e32 v168, v167
	v_cvt_f32_ubyte1_e32 v169, v167
	v_cvt_f32_ubyte2_e32 v172, v167
	v_cvt_f32_ubyte3_e32 v173, v167
	v_rcp_iflag_f32_e32 v166, v3
	v_rcp_iflag_f32_e32 v168, v168
	v_rcp_iflag_f32_e32 v167, v147
	v_rcp_iflag_f32_e32 v169, v169
	v_rcp_iflag_f32_e32 v170, v170
	v_rcp_iflag_f32_e32 v171, v171
	v_rcp_iflag_f32_e32 v172, v172
	v_rcp_iflag_f32_e32 v173, v173
	v_pk_mul_f32 v[156:157], v[166:167], v[156:157]
	v_pk_mul_f32 v[160:161], v[170:171], v[160:161]
	v_pk_mul_f32 v[154:155], v[168:169], v[154:155]
	v_pk_mul_f32 v[158:159], v[172:173], v[158:159]
	v_pk_mul_f32 v[132:133], v[132:133], v[160:161]
	v_pk_mul_f32 v[130:131], v[130:131], v[156:157]
	v_pk_mul_f32 v[128:129], v[128:129], v[158:159]
	v_pk_mul_f32 v[126:127], v[126:127], v[154:155]
; __device__ __forceinline__ u32x4 pack8(f32x4 v0, f32x4 v1) { u32x4 w; w.x = cvt_pk_bf16(v0[0], v0[1]); w.y = cvt_pk_bf16(v0[2], v0[3]); w.z = cvt_pk_bf16(v1[0], v1[1]); w.w = cvt_pk_bf16(v1[2], v1[3]); return w; }
; template <class T> __device__ __forceinline__ void est(T* p, T v) { if constexpr (MK_EPI_NT != 0) __builtin_nontemporal_store(v, p); else *p = v; }
;     __device__ __forceinline__ bool operator()(f32x4 (&acc)[2][2][4][2], const Unit& u, int wr, int wc, int fr, int fq) const {
;     ...
;         for (int ai = 0; ai < 2; ++ai)
; #pragma unroll
;             for (int m = 0; m < 4; ++m) { const int row = row0 + ai * 128 + m * 16;
; #pragma unroll
;                 for (int bj = 0; bj < 2; ++bj) { const int col = col0 + bj * 128; f32x4 g0, g1; unpack8_u8(*(const u32x2*)(G8 + (size_t)row * (NIN - C_G) + gc * DM + col), g0, g1);
;                     if (u.z < 2) { f32x4 h0, h1; unpack8_u8(*(const u32x2*)(G8 + (size_t)row * (NIN - C_G) + gn * DM + col), h0, h1);
; #pragma unroll
;                         for (int j = 0; j < 4; ++j) { g0[j] *= __builtin_amdgcn_rcpf(h0[j]); g1[j] *= __builtin_amdgcn_rcpf(h1[j]); }
;                         acc[ai][bj][m][0] *= g0; acc[ai][bj][m][1] *= g1;
;                     } else est((u32x4*)(mrgb + (size_t)row * DM + col), (u32x4)pack8(acc[ai][bj][m][0] * (g0 * (1.f / 255.f)), acc[ai][bj][m][1] * (g1 * (1.f / 255.f)))); } }
.LBB0_843:
	s_nop 0
	v_cndmask_b32_e64 v3, 0, 1, s[84:85]
	v_cmp_ne_u32_e64 s[0:1], 1, v3
	s_andn2_b64 vcc, exec, s[84:85]
	s_mov_b64 s[84:85], -1
	s_waitcnt vmcnt(14)
	v_mov_b32_e32 v160, v176
	v_mov_b32_e32 v161, v177
	s_mov_b32 s100, 0xc0000
	v_lshl_add_u64 v[212:213], v[208:209], 0, s[100:101]
	global_load_dwordx2 v[176:177], v[212:213], off offset:128
	s_mov_b32 s100, 0xc0000
	v_lshl_add_u64 v[214:215], v[210:211], 0, s[100:101]
	global_load_dwordx2 v[190:191], v[214:215], off
	v_cvt_f32_ubyte1_e32 v155, v160
	v_cvt_f32_ubyte0_e32 v154, v160
	v_cvt_f32_ubyte3_e32 v159, v160
	v_cvt_f32_ubyte2_e32 v158, v160
	v_cvt_f32_ubyte1_e32 v151, v161
	v_cvt_f32_ubyte0_e32 v150, v161
	v_cvt_f32_ubyte3_e32 v157, v161
	v_cvt_f32_ubyte2_e32 v156, v161
	s_cbranch_vccnz .LBB0_845
	v_pk_mul_f32 v[166:167], v[158:159], s[30:31] op_sel_hi:[1,0]
	v_pk_mul_f32 v[160:161], v[154:155], s[30:31] op_sel_hi:[1,0]
	v_pk_mul_f32 v[168:169], v[100:101], v[166:167]
	v_pk_mul_f32 v[166:167], v[150:151], s[30:31] op_sel_hi:[1,0]
	v_pk_mul_f32 v[170:171], v[156:157], s[30:31] op_sel_hi:[1,0]
	s_mov_b64 s[84:85], 0
	v_pk_mul_f32 v[160:161], v[98:99], v[160:161]
	v_pk_mul_f32 v[170:171], v[96:97], v[170:171]
	v_pk_mul_f32 v[172:173], v[94:95], v[166:167]
	v_cvt_pk_bf16_f32 v166, v160, v161
	v_cvt_pk_bf16_f32 v167, v168, v169
	s_nop 0
	v_cvt_pk_bf16_f32 v168, v172, v173
	v_cvt_pk_bf16_f32 v169, v170, v171
	global_store_dwordx4 v[148:149], v[166:169], off offset:256
.LBB0_845:
	s_andn2_b64 vcc, exec, s[84:85]
	s_cbranch_vccnz .LBB0_847
	s_nop 0
	s_waitcnt vmcnt(15)
	v_mov_b32_e32 v148, v192
	v_mov_b32_e32 v149, v193
	v_cvt_f32_ubyte0_e32 v3, v148
	v_cvt_f32_ubyte1_e32 v147, v148
	v_cvt_f32_ubyte2_e32 v160, v148
	v_cvt_f32_ubyte3_e32 v161, v148
	v_cvt_f32_ubyte0_e32 v152, v149
	v_cvt_f32_ubyte1_e32 v153, v149
	v_cvt_f32_ubyte2_e32 v166, v149
	v_cvt_f32_ubyte3_e32 v167, v149
	v_rcp_iflag_f32_e32 v148, v3
	v_rcp_iflag_f32_e32 v152, v152
	v_rcp_iflag_f32_e32 v149, v147
	v_rcp_iflag_f32_e32 v153, v153
	v_rcp_iflag_f32_e32 v160, v160
	v_rcp_iflag_f32_e32 v161, v161
	v_rcp_iflag_f32_e32 v166, v166
	v_rcp_iflag_f32_e32 v167, v167
	v_pk_mul_f32 v[148:149], v[148:149], v[154:155]
	v_pk_mul_f32 v[154:155], v[160:161], v[158:159]
	v_pk_mul_f32 v[150:151], v[152:153], v[150:151]
	v_pk_mul_f32 v[152:153], v[166:167], v[156:157]
	v_pk_mul_f32 v[100:101], v[100:101], v[154:155]
	v_pk_mul_f32 v[98:99], v[98:99], v[148:149]
	v_pk_mul_f32 v[96:97], v[96:97], v[152:153]
	v_pk_mul_f32 v[94:95], v[94:95], v[150:151]
.LBB0_847:
	v_or_b32_e32 v148, 16, v146
	v_mov_b64_e32 v[150:151], s[64:65]
	v_mad_i64_i32 v[152:153], s[38:39], v148, s88, v[150:151]
	v_lshl_add_u64 v[150:151], v[152:153], 0, s[8:9]
	v_lshl_add_u64 v[150:151], v[150:151], 0, v[4:5]
	s_nop 0
	v_ashrrev_i32_e32 v149, 31, v148
	v_lshlrev_b64 v[148:149], 12, v[148:149]
	v_lshl_add_u64 v[148:149], s[60:61], 0, v[148:149]
	s_mov_b64 s[84:85], -1
	s_and_b64 vcc, exec, s[0:1]
	v_lshl_add_u64 v[148:149], v[4:5], 1, v[148:149]
	s_waitcnt vmcnt(14)
	v_mov_b32_e32 v166, v178
	v_mov_b32_e32 v167, v179
	s_mov_b32 s100, 0xd8000
	v_lshl_add_u64 v[212:213], v[208:209], 0, s[100:101]
	global_load_dwordx2 v[178:179], v[212:213], off
	s_mov_b32 s100, 0xc0000
	v_lshl_add_u64 v[214:215], v[210:211], 0, s[100:101]
	global_load_dwordx2 v[192:193], v[214:215], off offset:128
	v_cvt_f32_ubyte1_e32 v157, v166
	v_cvt_f32_ubyte0_e32 v156, v166
	v_cvt_f32_ubyte3_e32 v161, v166
	v_cvt_f32_ubyte2_e32 v160, v166
	v_cvt_f32_ubyte1_e32 v155, v167
	v_cvt_f32_ubyte0_e32 v154, v167
	v_cvt_f32_ubyte3_e32 v159, v167
	v_cvt_f32_ubyte2_e32 v158, v167
	s_cbranch_vccnz .LBB0_849
	v_pk_mul_f32 v[166:167], v[156:157], s[30:31] op_sel_hi:[1,0]
	v_pk_mul_f32 v[168:169], v[160:161], s[30:31] op_sel_hi:[1,0]
	v_pk_mul_f32 v[166:167], v[122:123], v[166:167]
	v_pk_mul_f32 v[168:169], v[124:125], v[168:169]
	v_pk_mul_f32 v[170:171], v[154:155], s[30:31] op_sel_hi:[1,0]
	v_pk_mul_f32 v[172:173], v[158:159], s[30:31] op_sel_hi:[1,0]
	s_mov_b64 s[84:85], 0
	v_pk_mul_f32 v[172:173], v[120:121], v[172:173]
	v_pk_mul_f32 v[170:171], v[118:119], v[170:171]
	v_cvt_pk_bf16_f32 v166, v166, v167
	v_cvt_pk_bf16_f32 v167, v168, v169
	s_nop 0
	v_cvt_pk_bf16_f32 v168, v170, v171
	v_cvt_pk_bf16_f32 v169, v172, v173
	global_store_dwordx4 v[148:149], v[166:169], off
.LBB0_849:
	v_lshl_add_u64 v[152:153], v[152:153], 0, s[82:83]
	s_andn2_b64 vcc, exec, s[84:85]
	v_lshl_add_u64 v[152:153], v[152:153], 0, v[4:5]
	s_cbranch_vccnz .LBB0_851
	s_nop 0
	s_waitcnt vmcnt(15)
	v_mov_b32_e32 v166, v196
	v_mov_b32_e32 v167, v197
	v_cvt_f32_ubyte0_e32 v3, v166
	v_cvt_f32_ubyte1_e32 v147, v166
	v_cvt_f32_ubyte2_e32 v170, v166
	v_cvt_f32_ubyte3_e32 v171, v166
	v_cvt_f32_ubyte0_e32 v168, v167
	v_cvt_f32_ubyte1_e32 v169, v167
	v_cvt_f32_ubyte2_e32 v172, v167
	v_cvt_f32_ubyte3_e32 v173, v167
	v_rcp_iflag_f32_e32 v166, v3
	v_rcp_iflag_f32_e32 v168, v168
	v_rcp_iflag_f32_e32 v167, v147
	v_rcp_iflag_f32_e32 v169, v169
	v_rcp_iflag_f32_e32 v170, v170
	v_rcp_iflag_f32_e32 v171, v171
	v_rcp_iflag_f32_e32 v172, v172
	v_rcp_iflag_f32_e32 v173, v173
	v_pk_mul_f32 v[156:157], v[166:167], v[156:157]
	v_pk_mul_f32 v[160:161], v[170:171], v[160:161]
	v_pk_mul_f32 v[154:155], v[168:169], v[154:155]
	v_pk_mul_f32 v[158:159], v[172:173], v[158:159]
	v_pk_mul_f32 v[124:125], v[124:125], v[160:161]
	v_pk_mul_f32 v[122:123], v[122:123], v[156:157]
	v_pk_mul_f32 v[120:121], v[120:121], v[158:159]
	v_pk_mul_f32 v[118:119], v[118:119], v[154:155]
; __device__ __forceinline__ u32x4 pack8(f32x4 v0, f32x4 v1) { u32x4 w; w.x = cvt_pk_bf16(v0[0], v0[1]); w.y = cvt_pk_bf16(v0[2], v0[3]); w.z = cvt_pk_bf16(v1[0], v1[1]); w.w = cvt_pk_bf16(v1[2], v1[3]); return w; }
; template <class T> __device__ __forceinline__ void est(T* p, T v) { if constexpr (MK_EPI_NT != 0) __builtin_nontemporal_store(v, p); else *p = v; }
;     __device__ __forceinline__ bool operator()(f32x4 (&acc)[2][2][4][2], const Unit& u, int wr, int wc, int fr, int fq) const {
;     ...
;         for (int ai = 0; ai < 2; ++ai)
; #pragma unroll
;             for (int m = 0; m < 4; ++m) { const int row = row0 + ai * 128 + m * 16;
; #pragma unroll
;                 for (int bj = 0; bj < 2; ++bj) { const int col = col0 + bj * 128; f32x4 g0, g1; unpack8_u8(*(const u32x2*)(G8 + (size_t)row * (NIN - C_G) + gc * DM + col), g0, g1);
;                     if (u.z < 2) { f32x4 h0, h1; unpack8_u8(*(const u32x2*)(G8 + (size_t)row * (NIN - C_G) + gn * DM + col), h0, h1);
; #pragma unroll
;                         for (int j = 0; j < 4; ++j) { g0[j] *= __builtin_amdgcn_rcpf(h0[j]); g1[j] *= __builtin_amdgcn_rcpf(h1[j]); }
;                         acc[ai][bj][m][0] *= g0; acc[ai][bj][m][1] *= g1;
;                     } else est((u32x4*)(mrgb + (size_t)row * DM + col), (u32x4)pack8(acc[ai][bj][m][0] * (g0 * (1.f / 255.f)), acc[ai][bj][m][1] * (g1 * (1.f / 255.f)))); } }
.LBB0_851:
	s_nop 0
	s_and_b64 vcc, exec, s[0:1]
	s_mov_b64 s[84:85], -1
	s_waitcnt vmcnt(14)
	v_mov_b32_e32 v160, v180
	v_mov_b32_e32 v161, v181
	s_mov_b32 s100, 0xd8000
	v_lshl_add_u64 v[212:213], v[208:209], 0, s[100:101]
	global_load_dwordx2 v[180:181], v[212:213], off offset:128
	s_mov_b32 s100, 0xd8000
	v_lshl_add_u64 v[214:215], v[210:211], 0, s[100:101]
	global_load_dwordx2 v[196:197], v[214:215], off
	v_cvt_f32_ubyte1_e32 v155, v160
	v_cvt_f32_ubyte0_e32 v154, v160
	v_cvt_f32_ubyte3_e32 v159, v160
	v_cvt_f32_ubyte2_e32 v158, v160
	v_cvt_f32_ubyte1_e32 v151, v161
	v_cvt_f32_ubyte0_e32 v150, v161
	v_cvt_f32_ubyte3_e32 v157, v161
	v_cvt_f32_ubyte2_e32 v156, v161
	s_cbranch_vccnz .LBB0_853
	v_pk_mul_f32 v[166:167], v[158:159], s[30:31] op_sel_hi:[1,0]
	v_pk_mul_f32 v[160:161], v[154:155], s[30:31] op_sel_hi:[1,0]
	v_pk_mul_f32 v[168:169], v[92:93], v[166:167]
	v_pk_mul_f32 v[166:167], v[150:151], s[30:31] op_sel_hi:[1,0]
	v_pk_mul_f32 v[170:171], v[156:157], s[30:31] op_sel_hi:[1,0]
	s_mov_b64 s[84:85], 0
	v_pk_mul_f32 v[160:161], v[90:91], v[160:161]
	v_pk_mul_f32 v[170:171], v[88:89], v[170:171]
	v_pk_mul_f32 v[172:173], v[86:87], v[166:167]
	v_cvt_pk_bf16_f32 v166, v160, v161
	v_cvt_pk_bf16_f32 v167, v168, v169
	s_nop 0
	v_cvt_pk_bf16_f32 v168, v172, v173
	v_cvt_pk_bf16_f32 v169, v170, v171
	global_store_dwordx4 v[148:149], v[166:169], off offset:256
.LBB0_853:
	s_andn2_b64 vcc, exec, s[84:85]
	s_cbranch_vccnz .LBB0_855
	s_nop 0
	s_waitcnt vmcnt(15)
	v_mov_b32_e32 v148, v198
	v_mov_b32_e32 v149, v199
	v_cvt_f32_ubyte0_e32 v3, v148
	v_cvt_f32_ubyte1_e32 v147, v148
	v_cvt_f32_ubyte2_e32 v160, v148
	v_cvt_f32_ubyte3_e32 v161, v148
	v_cvt_f32_ubyte0_e32 v152, v149
	v_cvt_f32_ubyte1_e32 v153, v149
	v_cvt_f32_ubyte2_e32 v166, v149
	v_cvt_f32_ubyte3_e32 v167, v149
	v_rcp_iflag_f32_e32 v148, v3
	v_rcp_iflag_f32_e32 v152, v152
	v_rcp_iflag_f32_e32 v149, v147
	v_rcp_iflag_f32_e32 v153, v153
	v_rcp_iflag_f32_e32 v160, v160
	v_rcp_iflag_f32_e32 v161, v161
	v_rcp_iflag_f32_e32 v166, v166
	v_rcp_iflag_f32_e32 v167, v167
	v_pk_mul_f32 v[148:149], v[148:149], v[154:155]
	v_pk_mul_f32 v[154:155], v[160:161], v[158:159]
	v_pk_mul_f32 v[150:151], v[152:153], v[150:151]
	v_pk_mul_f32 v[152:153], v[166:167], v[156:157]
	v_pk_mul_f32 v[92:93], v[92:93], v[154:155]
	v_pk_mul_f32 v[90:91], v[90:91], v[148:149]
	v_pk_mul_f32 v[88:89], v[88:89], v[152:153]
	v_pk_mul_f32 v[86:87], v[86:87], v[150:151]
.LBB0_855:
	v_or_b32_e32 v148, 32, v146
	v_mov_b64_e32 v[150:151], s[64:65]
	v_mad_i64_i32 v[152:153], s[38:39], v148, s88, v[150:151]
	v_lshl_add_u64 v[150:151], v[152:153], 0, s[8:9]
	v_lshl_add_u64 v[150:151], v[150:151], 0, v[4:5]
	s_nop 0
	v_ashrrev_i32_e32 v149, 31, v148
	v_lshlrev_b64 v[148:149], 12, v[148:149]
	v_lshl_add_u64 v[148:149], s[60:61], 0, v[148:149]
	s_mov_b64 s[84:85], -1
	s_and_b64 vcc, exec, s[0:1]
	v_lshl_add_u64 v[148:149], v[4:5], 1, v[148:149]
	s_waitcnt vmcnt(14)
	v_mov_b32_e32 v166, v182
	v_mov_b32_e32 v167, v183
	s_mov_b32 s100, 0xf0000
	v_lshl_add_u64 v[212:213], v[208:209], 0, s[100:101]
	global_load_dwordx2 v[182:183], v[212:213], off
	s_mov_b32 s100, 0xd8000
	v_lshl_add_u64 v[214:215], v[210:211], 0, s[100:101]
	global_load_dwordx2 v[198:199], v[214:215], off offset:128
	v_cvt_f32_ubyte1_e32 v157, v166
	v_cvt_f32_ubyte0_e32 v156, v166
	v_cvt_f32_ubyte3_e32 v161, v166
	v_cvt_f32_ubyte2_e32 v160, v166
	v_cvt_f32_ubyte1_e32 v155, v167
	v_cvt_f32_ubyte0_e32 v154, v167
	v_cvt_f32_ubyte3_e32 v159, v167
	v_cvt_f32_ubyte2_e32 v158, v167
	s_cbranch_vccnz .LBB0_857
	v_pk_mul_f32 v[166:167], v[156:157], s[30:31] op_sel_hi:[1,0]
	v_pk_mul_f32 v[168:169], v[160:161], s[30:31] op_sel_hi:[1,0]
	v_pk_mul_f32 v[166:167], v[114:115], v[166:167]
	v_pk_mul_f32 v[168:169], v[116:117], v[168:169]
	v_pk_mul_f32 v[170:171], v[154:155], s[30:31] op_sel_hi:[1,0]
	v_pk_mul_f32 v[172:173], v[158:159], s[30:31] op_sel_hi:[1,0]
	s_mov_b64 s[84:85], 0
	v_pk_mul_f32 v[172:173], v[112:113], v[172:173]
	v_pk_mul_f32 v[170:171], v[110:111], v[170:171]
	v_cvt_pk_bf16_f32 v166, v166, v167
	v_cvt_pk_bf16_f32 v167, v168, v169
	s_nop 0
	v_cvt_pk_bf16_f32 v168, v170, v171
	v_cvt_pk_bf16_f32 v169, v172, v173
	global_store_dwordx4 v[148:149], v[166:169], off
.LBB0_857:
	v_lshl_add_u64 v[152:153], v[152:153], 0, s[82:83]
	s_andn2_b64 vcc, exec, s[84:85]
	v_lshl_add_u64 v[152:153], v[152:153], 0, v[4:5]
	s_cbranch_vccnz .LBB0_859
	s_nop 0
	s_waitcnt vmcnt(15)
	v_mov_b32_e32 v166, v200
	v_mov_b32_e32 v167, v201
	v_cvt_f32_ubyte0_e32 v3, v166
	v_cvt_f32_ubyte1_e32 v147, v166
	v_cvt_f32_ubyte2_e32 v170, v166
	v_cvt_f32_ubyte3_e32 v171, v166
	v_cvt_f32_ubyte0_e32 v168, v167
	v_cvt_f32_ubyte1_e32 v169, v167
	v_cvt_f32_ubyte2_e32 v172, v167
	v_cvt_f32_ubyte3_e32 v173, v167
	v_rcp_iflag_f32_e32 v166, v3
	v_rcp_iflag_f32_e32 v168, v168
	v_rcp_iflag_f32_e32 v167, v147
	v_rcp_iflag_f32_e32 v169, v169
	v_rcp_iflag_f32_e32 v170, v170
	v_rcp_iflag_f32_e32 v171, v171
	v_rcp_iflag_f32_e32 v172, v172
	v_rcp_iflag_f32_e32 v173, v173
	v_pk_mul_f32 v[156:157], v[166:167], v[156:157]
	v_pk_mul_f32 v[160:161], v[170:171], v[160:161]
	v_pk_mul_f32 v[154:155], v[168:169], v[154:155]
	v_pk_mul_f32 v[158:159], v[172:173], v[158:159]
	v_pk_mul_f32 v[116:117], v[116:117], v[160:161]
	v_pk_mul_f32 v[114:115], v[114:115], v[156:157]
	v_pk_mul_f32 v[112:113], v[112:113], v[158:159]
	v_pk_mul_f32 v[110:111], v[110:111], v[154:155]
; __device__ __forceinline__ u32x4 pack8(f32x4 v0, f32x4 v1) { u32x4 w; w.x = cvt_pk_bf16(v0[0], v0[1]); w.y = cvt_pk_bf16(v0[2], v0[3]); w.z = cvt_pk_bf16(v1[0], v1[1]); w.w = cvt_pk_bf16(v1[2], v1[3]); return w; }
; template <class T> __device__ __forceinline__ void est(T* p, T v) { if constexpr (MK_EPI_NT != 0) __builtin_nontemporal_store(v, p); else *p = v; }
;     __device__ __forceinline__ bool operator()(f32x4 (&acc)[2][2][4][2], const Unit& u, int wr, int wc, int fr, int fq) const {
;     ...
;         for (int ai = 0; ai < 2; ++ai)
; #pragma unroll
;             for (int m = 0; m < 4; ++m) { const int row = row0 + ai * 128 + m * 16;
; #pragma unroll
;                 for (int bj = 0; bj < 2; ++bj) { const int col = col0 + bj * 128; f32x4 g0, g1; unpack8_u8(*(const u32x2*)(G8 + (size_t)row * (NIN - C_G) + gc * DM + col), g0, g1);
;                     if (u.z < 2) { f32x4 h0, h1; unpack8_u8(*(const u32x2*)(G8 + (size_t)row * (NIN - C_G) + gn * DM + col), h0, h1);
; #pragma unroll
;                         for (int j = 0; j < 4; ++j) { g0[j] *= __builtin_amdgcn_rcpf(h0[j]); g1[j] *= __builtin_amdgcn_rcpf(h1[j]); }
;                         acc[ai][bj][m][0] *= g0; acc[ai][bj][m][1] *= g1;
;                     } else est((u32x4*)(mrgb + (size_t)row * DM + col), (u32x4)pack8(acc[ai][bj][m][0] * (g0 * (1.f / 255.f)), acc[ai][bj][m][1] * (g1 * (1.f / 255.f)))); } }
.LBB0_859:
	s_nop 0
	s_and_b64 vcc, exec, s[0:1]
	s_mov_b64 s[84:85], -1
	s_waitcnt vmcnt(14)
	v_mov_b32_e32 v160, v184
	v_mov_b32_e32 v161, v185
	s_mov_b32 s100, 0xf0000
	v_lshl_add_u64 v[212:213], v[208:209], 0, s[100:101]
	global_load_dwordx2 v[184:185], v[212:213], off offset:128
	s_mov_b32 s100, 0xf0000
	v_lshl_add_u64 v[214:215], v[210:211], 0, s[100:101]
	global_load_dwordx2 v[200:201], v[214:215], off
	v_cvt_f32_ubyte1_e32 v155, v160
	v_cvt_f32_ubyte0_e32 v154, v160
	v_cvt_f32_ubyte3_e32 v159, v160
	v_cvt_f32_ubyte2_e32 v158, v160
	v_cvt_f32_ubyte1_e32 v151, v161
	v_cvt_f32_ubyte0_e32 v150, v161
	v_cvt_f32_ubyte3_e32 v157, v161
	v_cvt_f32_ubyte2_e32 v156, v161
	s_cbranch_vccnz .LBB0_861
	v_pk_mul_f32 v[166:167], v[158:159], s[30:31] op_sel_hi:[1,0]
	v_pk_mul_f32 v[160:161], v[154:155], s[30:31] op_sel_hi:[1,0]
	v_pk_mul_f32 v[168:169], v[84:85], v[166:167]
	v_pk_mul_f32 v[166:167], v[150:151], s[30:31] op_sel_hi:[1,0]
	v_pk_mul_f32 v[170:171], v[156:157], s[30:31] op_sel_hi:[1,0]
	s_mov_b64 s[84:85], 0
	v_pk_mul_f32 v[160:161], v[82:83], v[160:161]
	v_pk_mul_f32 v[170:171], v[80:81], v[170:171]
	v_pk_mul_f32 v[172:173], v[78:79], v[166:167]
	v_cvt_pk_bf16_f32 v166, v160, v161
	v_cvt_pk_bf16_f32 v167, v168, v169
	s_nop 0
	v_cvt_pk_bf16_f32 v168, v172, v173
	v_cvt_pk_bf16_f32 v169, v170, v171
	global_store_dwordx4 v[148:149], v[166:169], off offset:256
.LBB0_861:
	s_andn2_b64 vcc, exec, s[84:85]
	s_cbranch_vccnz .LBB0_863
	s_nop 0
	s_waitcnt vmcnt(15)
	v_mov_b32_e32 v148, v202
	v_mov_b32_e32 v149, v203
	v_cvt_f32_ubyte0_e32 v3, v148
	v_cvt_f32_ubyte1_e32 v147, v148
	v_cvt_f32_ubyte2_e32 v160, v148
	v_cvt_f32_ubyte3_e32 v161, v148
	v_cvt_f32_ubyte0_e32 v152, v149
	v_cvt_f32_ubyte1_e32 v153, v149
	v_cvt_f32_ubyte2_e32 v166, v149
	v_cvt_f32_ubyte3_e32 v167, v149
	v_rcp_iflag_f32_e32 v148, v3
	v_rcp_iflag_f32_e32 v152, v152
	v_rcp_iflag_f32_e32 v149, v147
	v_rcp_iflag_f32_e32 v153, v153
	v_rcp_iflag_f32_e32 v160, v160
	v_rcp_iflag_f32_e32 v161, v161
	v_rcp_iflag_f32_e32 v166, v166
	v_rcp_iflag_f32_e32 v167, v167
	v_pk_mul_f32 v[148:149], v[148:149], v[154:155]
	v_pk_mul_f32 v[154:155], v[160:161], v[158:159]
	v_pk_mul_f32 v[150:151], v[152:153], v[150:151]
	v_pk_mul_f32 v[152:153], v[166:167], v[156:157]
	v_pk_mul_f32 v[84:85], v[84:85], v[154:155]
	v_pk_mul_f32 v[82:83], v[82:83], v[148:149]
	v_pk_mul_f32 v[80:81], v[80:81], v[152:153]
	v_pk_mul_f32 v[78:79], v[78:79], v[150:151]
.LBB0_863:
	v_or_b32_e32 v148, 48, v146
	v_mov_b64_e32 v[150:151], s[64:65]
	v_mad_i64_i32 v[152:153], s[38:39], v148, s88, v[150:151]
	v_lshl_add_u64 v[150:151], v[152:153], 0, s[8:9]
	v_lshl_add_u64 v[150:151], v[150:151], 0, v[4:5]
	s_nop 0
	v_ashrrev_i32_e32 v149, 31, v148
	v_lshlrev_b64 v[148:149], 12, v[148:149]
	v_lshl_add_u64 v[148:149], s[60:61], 0, v[148:149]
	s_mov_b64 s[84:85], -1
	s_and_b64 vcc, exec, s[0:1]
	v_lshl_add_u64 v[148:149], v[4:5], 1, v[148:149]
	s_waitcnt vmcnt(14)
	v_mov_b32_e32 v166, v186
	v_mov_b32_e32 v167, v187
	s_mov_b32 s100, 0x108000
	v_lshl_add_u64 v[212:213], v[208:209], 0, s[100:101]
	global_load_dwordx2 v[186:187], v[212:213], off
	s_mov_b32 s100, 0xf0000
	v_lshl_add_u64 v[214:215], v[210:211], 0, s[100:101]
	global_load_dwordx2 v[202:203], v[214:215], off offset:128
	v_cvt_f32_ubyte1_e32 v157, v166
	v_cvt_f32_ubyte0_e32 v156, v166
	v_cvt_f32_ubyte3_e32 v161, v166
	v_cvt_f32_ubyte2_e32 v160, v166
	v_cvt_f32_ubyte1_e32 v155, v167
	v_cvt_f32_ubyte0_e32 v154, v167
	v_cvt_f32_ubyte3_e32 v159, v167
	v_cvt_f32_ubyte2_e32 v158, v167
	s_cbranch_vccnz .LBB0_865
	v_pk_mul_f32 v[166:167], v[156:157], s[30:31] op_sel_hi:[1,0]
	v_pk_mul_f32 v[168:169], v[160:161], s[30:31] op_sel_hi:[1,0]
	v_pk_mul_f32 v[166:167], v[106:107], v[166:167]
	v_pk_mul_f32 v[168:169], v[108:109], v[168:169]
	v_pk_mul_f32 v[170:171], v[154:155], s[30:31] op_sel_hi:[1,0]
	v_pk_mul_f32 v[172:173], v[158:159], s[30:31] op_sel_hi:[1,0]
	s_mov_b64 s[84:85], 0
	v_pk_mul_f32 v[172:173], v[104:105], v[172:173]
	v_pk_mul_f32 v[170:171], v[102:103], v[170:171]
	v_cvt_pk_bf16_f32 v166, v166, v167
	v_cvt_pk_bf16_f32 v167, v168, v169
	s_nop 0
	v_cvt_pk_bf16_f32 v168, v170, v171
	v_cvt_pk_bf16_f32 v169, v172, v173
	global_store_dwordx4 v[148:149], v[166:169], off
.LBB0_865:
	v_lshl_add_u64 v[152:153], v[152:153], 0, s[82:83]
	s_andn2_b64 vcc, exec, s[84:85]
	v_lshl_add_u64 v[152:153], v[152:153], 0, v[4:5]
	s_cbranch_vccnz .LBB0_867
	s_nop 0
	s_waitcnt vmcnt(15)
	v_mov_b32_e32 v166, v204
	v_mov_b32_e32 v167, v205
	v_cvt_f32_ubyte0_e32 v3, v166
	v_cvt_f32_ubyte1_e32 v147, v166
	v_cvt_f32_ubyte2_e32 v170, v166
	v_cvt_f32_ubyte3_e32 v171, v166
	v_cvt_f32_ubyte0_e32 v168, v167
	v_cvt_f32_ubyte1_e32 v169, v167
	v_cvt_f32_ubyte2_e32 v172, v167
	v_cvt_f32_ubyte3_e32 v173, v167
	v_rcp_iflag_f32_e32 v166, v3
	v_rcp_iflag_f32_e32 v168, v168
	v_rcp_iflag_f32_e32 v167, v147
	v_rcp_iflag_f32_e32 v169, v169
	v_rcp_iflag_f32_e32 v170, v170
	v_rcp_iflag_f32_e32 v171, v171
	v_rcp_iflag_f32_e32 v172, v172
	v_rcp_iflag_f32_e32 v173, v173
	v_pk_mul_f32 v[156:157], v[166:167], v[156:157]
	v_pk_mul_f32 v[160:161], v[170:171], v[160:161]
	v_pk_mul_f32 v[154:155], v[168:169], v[154:155]
	v_pk_mul_f32 v[158:159], v[172:173], v[158:159]
	v_pk_mul_f32 v[108:109], v[108:109], v[160:161]
	v_pk_mul_f32 v[106:107], v[106:107], v[156:157]
	v_pk_mul_f32 v[104:105], v[104:105], v[158:159]
	v_pk_mul_f32 v[102:103], v[102:103], v[154:155]
; __device__ __forceinline__ u32x4 pack8(f32x4 v0, f32x4 v1) { u32x4 w; w.x = cvt_pk_bf16(v0[0], v0[1]); w.y = cvt_pk_bf16(v0[2], v0[3]); w.z = cvt_pk_bf16(v1[0], v1[1]); w.w = cvt_pk_bf16(v1[2], v1[3]); return w; }
; template <class T> __device__ __forceinline__ void est(T* p, T v) { if constexpr (MK_EPI_NT != 0) __builtin_nontemporal_store(v, p); else *p = v; }
;     __device__ __forceinline__ bool operator()(f32x4 (&acc)[2][2][4][2], const Unit& u, int wr, int wc, int fr, int fq) const {
;     ...
;         for (int ai = 0; ai < 2; ++ai)
; #pragma unroll
;             for (int m = 0; m < 4; ++m) { const int row = row0 + ai * 128 + m * 16;
; #pragma unroll
;                 for (int bj = 0; bj < 2; ++bj) { const int col = col0 + bj * 128; f32x4 g0, g1; unpack8_u8(*(const u32x2*)(G8 + (size_t)row * (NIN - C_G) + gc * DM + col), g0, g1);
;                     if (u.z < 2) { f32x4 h0, h1; unpack8_u8(*(const u32x2*)(G8 + (size_t)row * (NIN - C_G) + gn * DM + col), h0, h1);
; #pragma unroll
;                         for (int j = 0; j < 4; ++j) { g0[j] *= __builtin_amdgcn_rcpf(h0[j]); g1[j] *= __builtin_amdgcn_rcpf(h1[j]); }
;                         acc[ai][bj][m][0] *= g0; acc[ai][bj][m][1] *= g1;
;                     } else est((u32x4*)(mrgb + (size_t)row * DM + col), (u32x4)pack8(acc[ai][bj][m][0] * (g0 * (1.f / 255.f)), acc[ai][bj][m][1] * (g1 * (1.f / 255.f)))); } }
.LBB0_867:
	s_nop 0
	s_and_b64 vcc, exec, s[0:1]
	s_mov_b64 s[84:85], -1
	s_waitcnt vmcnt(14)
	v_mov_b32_e32 v160, v188
	v_mov_b32_e32 v161, v189
	s_mov_b32 s100, 0x108000
	v_lshl_add_u64 v[212:213], v[208:209], 0, s[100:101]
	global_load_dwordx2 v[188:189], v[212:213], off offset:128
	s_mov_b32 s100, 0x108000
	v_lshl_add_u64 v[214:215], v[210:211], 0, s[100:101]
	global_load_dwordx2 v[204:205], v[214:215], off
	v_cvt_f32_ubyte1_e32 v155, v160
	v_cvt_f32_ubyte0_e32 v154, v160
	v_cvt_f32_ubyte3_e32 v159, v160
	v_cvt_f32_ubyte2_e32 v158, v160
	v_cvt_f32_ubyte1_e32 v151, v161
	v_cvt_f32_ubyte0_e32 v150, v161
	v_cvt_f32_ubyte3_e32 v157, v161
	v_cvt_f32_ubyte2_e32 v156, v161
	s_cbranch_vccnz .LBB0_869
	v_pk_mul_f32 v[166:167], v[158:159], s[30:31] op_sel_hi:[1,0]
	v_pk_mul_f32 v[160:161], v[154:155], s[30:31] op_sel_hi:[1,0]
	v_pk_mul_f32 v[168:169], v[76:77], v[166:167]
	v_pk_mul_f32 v[166:167], v[150:151], s[30:31] op_sel_hi:[1,0]
	v_pk_mul_f32 v[170:171], v[156:157], s[30:31] op_sel_hi:[1,0]
	s_mov_b64 s[84:85], 0
	v_pk_mul_f32 v[160:161], v[74:75], v[160:161]
	v_pk_mul_f32 v[170:171], v[72:73], v[170:171]
	v_pk_mul_f32 v[172:173], v[70:71], v[166:167]
	v_cvt_pk_bf16_f32 v166, v160, v161
	v_cvt_pk_bf16_f32 v167, v168, v169
	s_nop 0
	v_cvt_pk_bf16_f32 v168, v172, v173
	v_cvt_pk_bf16_f32 v169, v170, v171
	global_store_dwordx4 v[148:149], v[166:169], off offset:256
.LBB0_869:
	s_andn2_b64 vcc, exec, s[84:85]
	s_cbranch_vccnz .LBB0_871
	s_nop 0
	s_waitcnt vmcnt(15)
	v_mov_b32_e32 v148, v206
	v_mov_b32_e32 v149, v207
	v_cvt_f32_ubyte0_e32 v3, v148
	v_cvt_f32_ubyte1_e32 v147, v148
	v_cvt_f32_ubyte2_e32 v160, v148
	v_cvt_f32_ubyte3_e32 v161, v148
	v_cvt_f32_ubyte0_e32 v152, v149
	v_cvt_f32_ubyte1_e32 v153, v149
	v_cvt_f32_ubyte2_e32 v166, v149
	v_cvt_f32_ubyte3_e32 v167, v149
	v_rcp_iflag_f32_e32 v148, v3
	v_rcp_iflag_f32_e32 v152, v152
	v_rcp_iflag_f32_e32 v149, v147
	v_rcp_iflag_f32_e32 v153, v153
	v_rcp_iflag_f32_e32 v160, v160
	v_rcp_iflag_f32_e32 v161, v161
	v_rcp_iflag_f32_e32 v166, v166
	v_rcp_iflag_f32_e32 v167, v167
	v_pk_mul_f32 v[148:149], v[148:149], v[154:155]
	v_pk_mul_f32 v[154:155], v[160:161], v[158:159]
	v_pk_mul_f32 v[150:151], v[152:153], v[150:151]
	v_pk_mul_f32 v[152:153], v[166:167], v[156:157]
	v_pk_mul_f32 v[76:77], v[76:77], v[154:155]
	v_pk_mul_f32 v[74:75], v[74:75], v[148:149]
	v_pk_mul_f32 v[72:73], v[72:73], v[152:153]
	v_pk_mul_f32 v[70:71], v[70:71], v[150:151]
.LBB0_871:
	v_add_u32_e32 v148, 0x80, v146
	v_mov_b64_e32 v[150:151], s[64:65]
	v_mad_i64_i32 v[152:153], s[38:39], v148, s88, v[150:151]
	v_lshl_add_u64 v[150:151], v[152:153], 0, s[8:9]
	v_lshl_add_u64 v[150:151], v[150:151], 0, v[4:5]
	s_nop 0
	v_ashrrev_i32_e32 v149, 31, v148
	v_lshlrev_b64 v[148:149], 12, v[148:149]
	v_lshl_add_u64 v[148:149], s[60:61], 0, v[148:149]
	s_mov_b64 s[84:85], -1
	s_and_b64 vcc, exec, s[0:1]
	v_lshl_add_u64 v[148:149], v[4:5], 1, v[148:149]
	s_waitcnt vmcnt(14)
	v_mov_b32_e32 v166, v174
	v_mov_b32_e32 v167, v175
	s_mov_b32 s100, 0x108000
	v_lshl_add_u64 v[214:215], v[210:211], 0, s[100:101]
	global_load_dwordx2 v[206:207], v[214:215], off offset:128
	v_cvt_f32_ubyte1_e32 v157, v166
	v_cvt_f32_ubyte0_e32 v156, v166
	v_cvt_f32_ubyte3_e32 v161, v166
	v_cvt_f32_ubyte2_e32 v160, v166
	v_cvt_f32_ubyte1_e32 v155, v167
	v_cvt_f32_ubyte0_e32 v154, v167
	v_cvt_f32_ubyte3_e32 v159, v167
	v_cvt_f32_ubyte2_e32 v158, v167
	s_cbranch_vccnz .LBB0_873
	v_pk_mul_f32 v[166:167], v[156:157], s[30:31] op_sel_hi:[1,0]
	v_pk_mul_f32 v[168:169], v[160:161], s[30:31] op_sel_hi:[1,0]
	v_pk_mul_f32 v[166:167], v[66:67], v[166:167]
	v_pk_mul_f32 v[168:169], v[68:69], v[168:169]
	v_pk_mul_f32 v[170:171], v[154:155], s[30:31] op_sel_hi:[1,0]
	v_pk_mul_f32 v[172:173], v[158:159], s[30:31] op_sel_hi:[1,0]
	s_mov_b64 s[84:85], 0
	v_pk_mul_f32 v[172:173], v[64:65], v[172:173]
	v_pk_mul_f32 v[170:171], v[62:63], v[170:171]
	v_cvt_pk_bf16_f32 v166, v166, v167
	v_cvt_pk_bf16_f32 v167, v168, v169
	s_nop 0
	v_cvt_pk_bf16_f32 v168, v170, v171
	v_cvt_pk_bf16_f32 v169, v172, v173
	global_store_dwordx4 v[148:149], v[166:169], off
.LBB0_873:
	v_lshl_add_u64 v[152:153], v[152:153], 0, s[82:83]
	s_andn2_b64 vcc, exec, s[84:85]
	v_lshl_add_u64 v[152:153], v[152:153], 0, v[4:5]
	s_cbranch_vccnz .LBB0_875
	s_nop 0
	s_waitcnt vmcnt(13)
	v_mov_b32_e32 v166, v190
	v_mov_b32_e32 v167, v191
	v_cvt_f32_ubyte0_e32 v3, v166
	v_cvt_f32_ubyte1_e32 v147, v166
	v_cvt_f32_ubyte2_e32 v170, v166
	v_cvt_f32_ubyte3_e32 v171, v166
	v_cvt_f32_ubyte0_e32 v168, v167
	v_cvt_f32_ubyte1_e32 v169, v167
	v_cvt_f32_ubyte2_e32 v172, v167
	v_cvt_f32_ubyte3_e32 v173, v167
	v_rcp_iflag_f32_e32 v166, v3
	v_rcp_iflag_f32_e32 v168, v168
	v_rcp_iflag_f32_e32 v167, v147
	v_rcp_iflag_f32_e32 v169, v169
	v_rcp_iflag_f32_e32 v170, v170
	v_rcp_iflag_f32_e32 v171, v171
	v_rcp_iflag_f32_e32 v172, v172
	v_rcp_iflag_f32_e32 v173, v173
	v_pk_mul_f32 v[156:157], v[166:167], v[156:157]
	v_pk_mul_f32 v[160:161], v[170:171], v[160:161]
	v_pk_mul_f32 v[154:155], v[168:169], v[154:155]
	v_pk_mul_f32 v[158:159], v[172:173], v[158:159]
	v_pk_mul_f32 v[68:69], v[68:69], v[160:161]
	v_pk_mul_f32 v[66:67], v[66:67], v[156:157]
	v_pk_mul_f32 v[64:65], v[64:65], v[158:159]
	v_pk_mul_f32 v[62:63], v[62:63], v[154:155]
; __device__ __forceinline__ u32x4 pack8(f32x4 v0, f32x4 v1) { u32x4 w; w.x = cvt_pk_bf16(v0[0], v0[1]); w.y = cvt_pk_bf16(v0[2], v0[3]); w.z = cvt_pk_bf16(v1[0], v1[1]); w.w = cvt_pk_bf16(v1[2], v1[3]); return w; }
; template <class T> __device__ __forceinline__ void est(T* p, T v) { if constexpr (MK_EPI_NT != 0) __builtin_nontemporal_store(v, p); else *p = v; }
;     __device__ __forceinline__ bool operator()(f32x4 (&acc)[2][2][4][2], const Unit& u, int wr, int wc, int fr, int fq) const {
;     ...
;         for (int ai = 0; ai < 2; ++ai)
; #pragma unroll
;             for (int m = 0; m < 4; ++m) { const int row = row0 + ai * 128 + m * 16;
; #pragma unroll
;                 for (int bj = 0; bj < 2; ++bj) { const int col = col0 + bj * 128; f32x4 g0, g1; unpack8_u8(*(const u32x2*)(G8 + (size_t)row * (NIN - C_G) + gc * DM + col), g0, g1);
;                     if (u.z < 2) { f32x4 h0, h1; unpack8_u8(*(const u32x2*)(G8 + (size_t)row * (NIN - C_G) + gn * DM + col), h0, h1);
; #pragma unroll
;                         for (int j = 0; j < 4; ++j) { g0[j] *= __builtin_amdgcn_rcpf(h0[j]); g1[j] *= __builtin_amdgcn_rcpf(h1[j]); }
;                         acc[ai][bj][m][0] *= g0; acc[ai][bj][m][1] *= g1;
;                     } else est((u32x4*)(mrgb + (size_t)row * DM + col), (u32x4)pack8(acc[ai][bj][m][0] * (g0 * (1.f / 255.f)), acc[ai][bj][m][1] * (g1 * (1.f / 255.f)))); } }
.LBB0_875:
	s_nop 0
	s_and_b64 vcc, exec, s[0:1]
	s_mov_b64 s[84:85], -1
	s_waitcnt vmcnt(14)
	v_mov_b32_e32 v160, v176
	v_mov_b32_e32 v161, v177
	v_cvt_f32_ubyte1_e32 v155, v160
	v_cvt_f32_ubyte0_e32 v154, v160
	v_cvt_f32_ubyte3_e32 v159, v160
	v_cvt_f32_ubyte2_e32 v158, v160
	v_cvt_f32_ubyte1_e32 v151, v161
	v_cvt_f32_ubyte0_e32 v150, v161
	v_cvt_f32_ubyte3_e32 v157, v161
	v_cvt_f32_ubyte2_e32 v156, v161
	s_cbranch_vccnz .LBB0_877
	v_pk_mul_f32 v[166:167], v[158:159], s[30:31] op_sel_hi:[1,0]
	v_pk_mul_f32 v[160:161], v[154:155], s[30:31] op_sel_hi:[1,0]
	v_pk_mul_f32 v[168:169], v[36:37], v[166:167]
	v_pk_mul_f32 v[166:167], v[150:151], s[30:31] op_sel_hi:[1,0]
	v_pk_mul_f32 v[170:171], v[156:157], s[30:31] op_sel_hi:[1,0]
	s_mov_b64 s[84:85], 0
	v_pk_mul_f32 v[160:161], v[34:35], v[160:161]
	v_pk_mul_f32 v[170:171], v[32:33], v[170:171]
	v_pk_mul_f32 v[172:173], v[30:31], v[166:167]
	v_cvt_pk_bf16_f32 v166, v160, v161
	v_cvt_pk_bf16_f32 v167, v168, v169
	s_nop 0
	v_cvt_pk_bf16_f32 v168, v172, v173
	v_cvt_pk_bf16_f32 v169, v170, v171
	global_store_dwordx4 v[148:149], v[166:169], off offset:256
.LBB0_877:
	s_andn2_b64 vcc, exec, s[84:85]
	s_cbranch_vccnz .LBB0_879
	s_nop 0
	s_waitcnt vmcnt(11)
	v_mov_b32_e32 v148, v192
	v_mov_b32_e32 v149, v193
	v_cvt_f32_ubyte0_e32 v3, v148
	v_cvt_f32_ubyte1_e32 v147, v148
	v_cvt_f32_ubyte2_e32 v160, v148
	v_cvt_f32_ubyte3_e32 v161, v148
	v_cvt_f32_ubyte0_e32 v152, v149
	v_cvt_f32_ubyte1_e32 v153, v149
	v_cvt_f32_ubyte2_e32 v166, v149
	v_cvt_f32_ubyte3_e32 v167, v149
	v_rcp_iflag_f32_e32 v148, v3
	v_rcp_iflag_f32_e32 v152, v152
	v_rcp_iflag_f32_e32 v149, v147
	v_rcp_iflag_f32_e32 v153, v153
	v_rcp_iflag_f32_e32 v160, v160
	v_rcp_iflag_f32_e32 v161, v161
	v_rcp_iflag_f32_e32 v166, v166
	v_rcp_iflag_f32_e32 v167, v167
	v_pk_mul_f32 v[148:149], v[148:149], v[154:155]
	v_pk_mul_f32 v[154:155], v[160:161], v[158:159]
	v_pk_mul_f32 v[150:151], v[152:153], v[150:151]
	v_pk_mul_f32 v[152:153], v[166:167], v[156:157]
	v_pk_mul_f32 v[36:37], v[36:37], v[154:155]
	v_pk_mul_f32 v[34:35], v[34:35], v[148:149]
	v_pk_mul_f32 v[32:33], v[32:33], v[152:153]
	v_pk_mul_f32 v[30:31], v[30:31], v[150:151]
.LBB0_879:
	v_add_u32_e32 v148, 0x90, v146
	v_mov_b64_e32 v[150:151], s[64:65]
	v_mad_i64_i32 v[152:153], s[38:39], v148, s88, v[150:151]
	v_lshl_add_u64 v[150:151], v[152:153], 0, s[8:9]
	v_lshl_add_u64 v[150:151], v[150:151], 0, v[4:5]
	s_nop 0
	v_ashrrev_i32_e32 v149, 31, v148
	v_lshlrev_b64 v[148:149], 12, v[148:149]
	v_lshl_add_u64 v[148:149], s[60:61], 0, v[148:149]
	s_mov_b64 s[84:85], -1
	s_and_b64 vcc, exec, s[0:1]
	v_lshl_add_u64 v[148:149], v[4:5], 1, v[148:149]
	s_waitcnt vmcnt(12)
	v_mov_b32_e32 v166, v178
	v_mov_b32_e32 v167, v179
	v_cvt_f32_ubyte1_e32 v157, v166
	v_cvt_f32_ubyte0_e32 v156, v166
	v_cvt_f32_ubyte3_e32 v161, v166
	v_cvt_f32_ubyte2_e32 v160, v166
	v_cvt_f32_ubyte1_e32 v155, v167
	v_cvt_f32_ubyte0_e32 v154, v167
	v_cvt_f32_ubyte3_e32 v159, v167
	v_cvt_f32_ubyte2_e32 v158, v167
	s_cbranch_vccnz .LBB0_881
	v_pk_mul_f32 v[166:167], v[156:157], s[30:31] op_sel_hi:[1,0]
	v_pk_mul_f32 v[168:169], v[160:161], s[30:31] op_sel_hi:[1,0]
	v_pk_mul_f32 v[166:167], v[58:59], v[166:167]
	v_pk_mul_f32 v[168:169], v[60:61], v[168:169]
	v_pk_mul_f32 v[170:171], v[154:155], s[30:31] op_sel_hi:[1,0]
	v_pk_mul_f32 v[172:173], v[158:159], s[30:31] op_sel_hi:[1,0]
	s_mov_b64 s[84:85], 0
	v_pk_mul_f32 v[172:173], v[56:57], v[172:173]
	v_pk_mul_f32 v[170:171], v[54:55], v[170:171]
	v_cvt_pk_bf16_f32 v166, v166, v167
	v_cvt_pk_bf16_f32 v167, v168, v169
	s_nop 0
	v_cvt_pk_bf16_f32 v168, v170, v171
	v_cvt_pk_bf16_f32 v169, v172, v173
	global_store_dwordx4 v[148:149], v[166:169], off
.LBB0_881:
	v_lshl_add_u64 v[152:153], v[152:153], 0, s[82:83]
	s_andn2_b64 vcc, exec, s[84:85]
	v_lshl_add_u64 v[152:153], v[152:153], 0, v[4:5]
	s_cbranch_vccnz .LBB0_883
	s_nop 0
	s_waitcnt vmcnt(9)
	v_mov_b32_e32 v166, v196
	v_mov_b32_e32 v167, v197
	v_cvt_f32_ubyte0_e32 v3, v166
	v_cvt_f32_ubyte1_e32 v147, v166
	v_cvt_f32_ubyte2_e32 v170, v166
	v_cvt_f32_ubyte3_e32 v171, v166
	v_cvt_f32_ubyte0_e32 v168, v167
	v_cvt_f32_ubyte1_e32 v169, v167
	v_cvt_f32_ubyte2_e32 v172, v167
	v_cvt_f32_ubyte3_e32 v173, v167
	v_rcp_iflag_f32_e32 v166, v3
	v_rcp_iflag_f32_e32 v168, v168
	v_rcp_iflag_f32_e32 v167, v147
	v_rcp_iflag_f32_e32 v169, v169
	v_rcp_iflag_f32_e32 v170, v170
	v_rcp_iflag_f32_e32 v171, v171
	v_rcp_iflag_f32_e32 v172, v172
	v_rcp_iflag_f32_e32 v173, v173
	v_pk_mul_f32 v[156:157], v[166:167], v[156:157]
	v_pk_mul_f32 v[160:161], v[170:171], v[160:161]
	v_pk_mul_f32 v[154:155], v[168:169], v[154:155]
	v_pk_mul_f32 v[158:159], v[172:173], v[158:159]
	v_pk_mul_f32 v[60:61], v[60:61], v[160:161]
	v_pk_mul_f32 v[58:59], v[58:59], v[156:157]
	v_pk_mul_f32 v[56:57], v[56:57], v[158:159]
	v_pk_mul_f32 v[54:55], v[54:55], v[154:155]
.LBB0_883:
	s_nop 0
	s_and_b64 vcc, exec, s[0:1]
	s_mov_b64 s[84:85], -1
	s_waitcnt vmcnt(10)
	v_mov_b32_e32 v160, v180
	v_mov_b32_e32 v161, v181
	v_cvt_f32_ubyte1_e32 v155, v160
	v_cvt_f32_ubyte0_e32 v154, v160
	v_cvt_f32_ubyte3_e32 v159, v160
	v_cvt_f32_ubyte2_e32 v158, v160
	v_cvt_f32_ubyte1_e32 v151, v161
	v_cvt_f32_ubyte0_e32 v150, v161
	v_cvt_f32_ubyte3_e32 v157, v161
	v_cvt_f32_ubyte2_e32 v156, v161
	s_cbranch_vccnz .LBB0_885
	v_pk_mul_f32 v[166:167], v[158:159], s[30:31] op_sel_hi:[1,0]
	v_pk_mul_f32 v[160:161], v[154:155], s[30:31] op_sel_hi:[1,0]
	v_pk_mul_f32 v[168:169], v[28:29], v[166:167]
	v_pk_mul_f32 v[166:167], v[150:151], s[30:31] op_sel_hi:[1,0]
	v_pk_mul_f32 v[170:171], v[156:157], s[30:31] op_sel_hi:[1,0]
	s_mov_b64 s[84:85], 0
	v_pk_mul_f32 v[160:161], v[26:27], v[160:161]
	v_pk_mul_f32 v[170:171], v[24:25], v[170:171]
	v_pk_mul_f32 v[172:173], v[22:23], v[166:167]
	v_cvt_pk_bf16_f32 v166, v160, v161
	v_cvt_pk_bf16_f32 v167, v168, v169
	s_nop 0
	v_cvt_pk_bf16_f32 v168, v172, v173
	v_cvt_pk_bf16_f32 v169, v170, v171
	global_store_dwordx4 v[148:149], v[166:169], off offset:256
; __device__ __forceinline__ u32x4 pack8(f32x4 v0, f32x4 v1) { u32x4 w; w.x = cvt_pk_bf16(v0[0], v0[1]); w.y = cvt_pk_bf16(v0[2], v0[3]); w.z = cvt_pk_bf16(v1[0], v1[1]); w.w = cvt_pk_bf16(v1[2], v1[3]); return w; }
; template <class T> __device__ __forceinline__ void est(T* p, T v) { if constexpr (MK_EPI_NT != 0) __builtin_nontemporal_store(v, p); else *p = v; }
;     __device__ __forceinline__ bool operator()(f32x4 (&acc)[2][2][4][2], const Unit& u, int wr, int wc, int fr, int fq) const {
;     ...
;         for (int ai = 0; ai < 2; ++ai)
; #pragma unroll
;             for (int m = 0; m < 4; ++m) { const int row = row0 + ai * 128 + m * 16;
; #pragma unroll
;                 for (int bj = 0; bj < 2; ++bj) { const int col = col0 + bj * 128; f32x4 g0, g1; unpack8_u8(*(const u32x2*)(G8 + (size_t)row * (NIN - C_G) + gc * DM + col), g0, g1);
;                     if (u.z < 2) { f32x4 h0, h1; unpack8_u8(*(const u32x2*)(G8 + (size_t)row * (NIN - C_G) + gn * DM + col), h0, h1);
; #pragma unroll
;                         for (int j = 0; j < 4; ++j) { g0[j] *= __builtin_amdgcn_rcpf(h0[j]); g1[j] *= __builtin_amdgcn_rcpf(h1[j]); }
;                         acc[ai][bj][m][0] *= g0; acc[ai][bj][m][1] *= g1;
;                     } else est((u32x4*)(mrgb + (size_t)row * DM + col), (u32x4)pack8(acc[ai][bj][m][0] * (g0 * (1.f / 255.f)), acc[ai][bj][m][1] * (g1 * (1.f / 255.f)))); } }
.LBB0_885:
	s_andn2_b64 vcc, exec, s[84:85]
	s_cbranch_vccnz .LBB0_887
	s_nop 0
	s_waitcnt vmcnt(7)
	v_mov_b32_e32 v148, v198
	v_mov_b32_e32 v149, v199
	v_cvt_f32_ubyte0_e32 v3, v148
	v_cvt_f32_ubyte1_e32 v147, v148
	v_cvt_f32_ubyte2_e32 v160, v148
	v_cvt_f32_ubyte3_e32 v161, v148
	v_cvt_f32_ubyte0_e32 v152, v149
	v_cvt_f32_ubyte1_e32 v153, v149
	v_cvt_f32_ubyte2_e32 v166, v149
	v_cvt_f32_ubyte3_e32 v167, v149
	v_rcp_iflag_f32_e32 v148, v3
	v_rcp_iflag_f32_e32 v152, v152
	v_rcp_iflag_f32_e32 v149, v147
	v_rcp_iflag_f32_e32 v153, v153
	v_rcp_iflag_f32_e32 v160, v160
	v_rcp_iflag_f32_e32 v161, v161
	v_rcp_iflag_f32_e32 v166, v166
	v_rcp_iflag_f32_e32 v167, v167
	v_pk_mul_f32 v[148:149], v[148:149], v[154:155]
	v_pk_mul_f32 v[154:155], v[160:161], v[158:159]
	v_pk_mul_f32 v[150:151], v[152:153], v[150:151]
	v_pk_mul_f32 v[152:153], v[166:167], v[156:157]
	v_pk_mul_f32 v[28:29], v[28:29], v[154:155]
	v_pk_mul_f32 v[26:27], v[26:27], v[148:149]
	v_pk_mul_f32 v[24:25], v[24:25], v[152:153]
	v_pk_mul_f32 v[22:23], v[22:23], v[150:151]
.LBB0_887:
	v_add_u32_e32 v148, 0xa0, v146
	v_mov_b64_e32 v[150:151], s[64:65]
	v_mad_i64_i32 v[152:153], s[38:39], v148, s88, v[150:151]
	v_lshl_add_u64 v[150:151], v[152:153], 0, s[8:9]
	v_lshl_add_u64 v[150:151], v[150:151], 0, v[4:5]
	s_nop 0
	v_ashrrev_i32_e32 v149, 31, v148
	v_lshlrev_b64 v[148:149], 12, v[148:149]
	v_lshl_add_u64 v[148:149], s[60:61], 0, v[148:149]
	s_mov_b64 s[84:85], -1
	s_and_b64 vcc, exec, s[0:1]
	v_lshl_add_u64 v[148:149], v[4:5], 1, v[148:149]
	s_waitcnt vmcnt(8)
	v_mov_b32_e32 v166, v182
	v_mov_b32_e32 v167, v183
	v_cvt_f32_ubyte1_e32 v157, v166
	v_cvt_f32_ubyte0_e32 v156, v166
	v_cvt_f32_ubyte3_e32 v161, v166
	v_cvt_f32_ubyte2_e32 v160, v166
	v_cvt_f32_ubyte1_e32 v155, v167
	v_cvt_f32_ubyte0_e32 v154, v167
	v_cvt_f32_ubyte3_e32 v159, v167
	v_cvt_f32_ubyte2_e32 v158, v167
	s_cbranch_vccnz .LBB0_889
	v_pk_mul_f32 v[166:167], v[156:157], s[30:31] op_sel_hi:[1,0]
	v_pk_mul_f32 v[168:169], v[160:161], s[30:31] op_sel_hi:[1,0]
	v_pk_mul_f32 v[166:167], v[50:51], v[166:167]
	v_pk_mul_f32 v[168:169], v[52:53], v[168:169]
	v_pk_mul_f32 v[170:171], v[154:155], s[30:31] op_sel_hi:[1,0]
	v_pk_mul_f32 v[172:173], v[158:159], s[30:31] op_sel_hi:[1,0]
	s_mov_b64 s[84:85], 0
	v_pk_mul_f32 v[172:173], v[48:49], v[172:173]
	v_pk_mul_f32 v[170:171], v[46:47], v[170:171]
	v_cvt_pk_bf16_f32 v166, v166, v167
	v_cvt_pk_bf16_f32 v167, v168, v169
	s_nop 0
	v_cvt_pk_bf16_f32 v168, v170, v171
	v_cvt_pk_bf16_f32 v169, v172, v173
	global_store_dwordx4 v[148:149], v[166:169], off
.LBB0_889:
	v_lshl_add_u64 v[152:153], v[152:153], 0, s[82:83]
	s_andn2_b64 vcc, exec, s[84:85]
	v_lshl_add_u64 v[152:153], v[152:153], 0, v[4:5]
	s_cbranch_vccnz .LBB0_891
	s_nop 0
	s_waitcnt vmcnt(5)
	v_mov_b32_e32 v166, v200
	v_mov_b32_e32 v167, v201
	v_cvt_f32_ubyte0_e32 v3, v166
	v_cvt_f32_ubyte1_e32 v147, v166
	v_cvt_f32_ubyte2_e32 v170, v166
	v_cvt_f32_ubyte3_e32 v171, v166
	v_cvt_f32_ubyte0_e32 v168, v167
	v_cvt_f32_ubyte1_e32 v169, v167
	v_cvt_f32_ubyte2_e32 v172, v167
	v_cvt_f32_ubyte3_e32 v173, v167
	v_rcp_iflag_f32_e32 v166, v3
	v_rcp_iflag_f32_e32 v168, v168
	v_rcp_iflag_f32_e32 v167, v147
	v_rcp_iflag_f32_e32 v169, v169
	v_rcp_iflag_f32_e32 v170, v170
	v_rcp_iflag_f32_e32 v171, v171
	v_rcp_iflag_f32_e32 v172, v172
	v_rcp_iflag_f32_e32 v173, v173
	v_pk_mul_f32 v[156:157], v[166:167], v[156:157]
	v_pk_mul_f32 v[160:161], v[170:171], v[160:161]
	v_pk_mul_f32 v[154:155], v[168:169], v[154:155]
	v_pk_mul_f32 v[158:159], v[172:173], v[158:159]
	v_pk_mul_f32 v[52:53], v[52:53], v[160:161]
	v_pk_mul_f32 v[50:51], v[50:51], v[156:157]
	v_pk_mul_f32 v[48:49], v[48:49], v[158:159]
	v_pk_mul_f32 v[46:47], v[46:47], v[154:155]
.LBB0_891:
	s_nop 0
	s_and_b64 vcc, exec, s[0:1]
	s_mov_b64 s[84:85], -1
	s_waitcnt vmcnt(6)
	v_mov_b32_e32 v160, v184
	v_mov_b32_e32 v161, v185
	v_cvt_f32_ubyte1_e32 v155, v160
	v_cvt_f32_ubyte0_e32 v154, v160
	v_cvt_f32_ubyte3_e32 v159, v160
	v_cvt_f32_ubyte2_e32 v158, v160
	v_cvt_f32_ubyte1_e32 v151, v161
	v_cvt_f32_ubyte0_e32 v150, v161
	v_cvt_f32_ubyte3_e32 v157, v161
	v_cvt_f32_ubyte2_e32 v156, v161
	s_cbranch_vccnz .LBB0_893
	v_pk_mul_f32 v[166:167], v[158:159], s[30:31] op_sel_hi:[1,0]
	v_pk_mul_f32 v[160:161], v[154:155], s[30:31] op_sel_hi:[1,0]
	v_pk_mul_f32 v[168:169], v[20:21], v[166:167]
	v_pk_mul_f32 v[166:167], v[150:151], s[30:31] op_sel_hi:[1,0]
	v_pk_mul_f32 v[170:171], v[156:157], s[30:31] op_sel_hi:[1,0]
	s_mov_b64 s[84:85], 0
	v_pk_mul_f32 v[160:161], v[18:19], v[160:161]
	v_pk_mul_f32 v[170:171], v[16:17], v[170:171]
	v_pk_mul_f32 v[172:173], v[14:15], v[166:167]
	v_cvt_pk_bf16_f32 v166, v160, v161
	v_cvt_pk_bf16_f32 v167, v168, v169
	s_nop 0
	v_cvt_pk_bf16_f32 v168, v172, v173
	v_cvt_pk_bf16_f32 v169, v170, v171
	global_store_dwordx4 v[148:149], v[166:169], off offset:256
; __device__ __forceinline__ u32x4 pack8(f32x4 v0, f32x4 v1) { u32x4 w; w.x = cvt_pk_bf16(v0[0], v0[1]); w.y = cvt_pk_bf16(v0[2], v0[3]); w.z = cvt_pk_bf16(v1[0], v1[1]); w.w = cvt_pk_bf16(v1[2], v1[3]); return w; }
; template <class T> __device__ __forceinline__ void est(T* p, T v) { if constexpr (MK_EPI_NT != 0) __builtin_nontemporal_store(v, p); else *p = v; }
;     __device__ __forceinline__ bool operator()(f32x4 (&acc)[2][2][4][2], const Unit& u, int wr, int wc, int fr, int fq) const {
;     ...
;         for (int ai = 0; ai < 2; ++ai)
; #pragma unroll
;             for (int m = 0; m < 4; ++m) { const int row = row0 + ai * 128 + m * 16;
; #pragma unroll
;                 for (int bj = 0; bj < 2; ++bj) { const int col = col0 + bj * 128; f32x4 g0, g1; unpack8_u8(*(const u32x2*)(G8 + (size_t)row * (NIN - C_G) + gc * DM + col), g0, g1);
;                     if (u.z < 2) { f32x4 h0, h1; unpack8_u8(*(const u32x2*)(G8 + (size_t)row * (NIN - C_G) + gn * DM + col), h0, h1);
; #pragma unroll
;                         for (int j = 0; j < 4; ++j) { g0[j] *= __builtin_amdgcn_rcpf(h0[j]); g1[j] *= __builtin_amdgcn_rcpf(h1[j]); }
;                         acc[ai][bj][m][0] *= g0; acc[ai][bj][m][1] *= g1;
;                     } else est((u32x4*)(mrgb + (size_t)row * DM + col), (u32x4)pack8(acc[ai][bj][m][0] * (g0 * (1.f / 255.f)), acc[ai][bj][m][1] * (g1 * (1.f / 255.f)))); } }
.LBB0_893:
	s_andn2_b64 vcc, exec, s[84:85]
	s_cbranch_vccnz .LBB0_895
	s_nop 0
	s_waitcnt vmcnt(3)
	v_mov_b32_e32 v148, v202
	v_mov_b32_e32 v149, v203
	v_cvt_f32_ubyte0_e32 v3, v148
	v_cvt_f32_ubyte1_e32 v147, v148
	v_cvt_f32_ubyte2_e32 v160, v148
	v_cvt_f32_ubyte3_e32 v161, v148
	v_cvt_f32_ubyte0_e32 v152, v149
	v_cvt_f32_ubyte1_e32 v153, v149
	v_cvt_f32_ubyte2_e32 v166, v149
	v_cvt_f32_ubyte3_e32 v167, v149
	v_rcp_iflag_f32_e32 v148, v3
	v_rcp_iflag_f32_e32 v152, v152
	v_rcp_iflag_f32_e32 v149, v147
	v_rcp_iflag_f32_e32 v153, v153
	v_rcp_iflag_f32_e32 v160, v160
	v_rcp_iflag_f32_e32 v161, v161
	v_rcp_iflag_f32_e32 v166, v166
	v_rcp_iflag_f32_e32 v167, v167
	v_pk_mul_f32 v[148:149], v[148:149], v[154:155]
	v_pk_mul_f32 v[154:155], v[160:161], v[158:159]
	v_pk_mul_f32 v[150:151], v[152:153], v[150:151]
	v_pk_mul_f32 v[152:153], v[166:167], v[156:157]
	v_pk_mul_f32 v[20:21], v[20:21], v[154:155]
	v_pk_mul_f32 v[18:19], v[18:19], v[148:149]
	v_pk_mul_f32 v[16:17], v[16:17], v[152:153]
	v_pk_mul_f32 v[14:15], v[14:15], v[150:151]
.LBB0_895:
	v_add_u32_e32 v146, 0xb0, v146
	v_mov_b64_e32 v[148:149], s[64:65]
	v_mad_i64_i32 v[158:159], s[38:39], v146, s88, v[148:149]
	v_lshl_add_u64 v[148:149], v[158:159], 0, s[8:9]
	v_lshl_add_u64 v[148:149], v[148:149], 0, v[4:5]
	s_nop 0
	v_ashrrev_i32_e32 v147, 31, v146
	v_lshlrev_b64 v[146:147], 12, v[146:147]
	v_lshl_add_u64 v[146:147], s[60:61], 0, v[146:147]
	s_mov_b64 s[84:85], -1
	s_and_b64 vcc, exec, s[0:1]
	v_lshl_add_u64 v[146:147], v[4:5], 1, v[146:147]
	s_waitcnt vmcnt(4)
	v_mov_b32_e32 v160, v186
	v_mov_b32_e32 v161, v187
	v_cvt_f32_ubyte1_e32 v153, v160
	v_cvt_f32_ubyte0_e32 v152, v160
	v_cvt_f32_ubyte3_e32 v157, v160
	v_cvt_f32_ubyte2_e32 v156, v160
	v_cvt_f32_ubyte1_e32 v151, v161
	v_cvt_f32_ubyte0_e32 v150, v161
	v_cvt_f32_ubyte3_e32 v155, v161
	v_cvt_f32_ubyte2_e32 v154, v161
	s_cbranch_vccnz .LBB0_897
	v_pk_mul_f32 v[166:167], v[156:157], s[30:31] op_sel_hi:[1,0]
	v_pk_mul_f32 v[160:161], v[152:153], s[30:31] op_sel_hi:[1,0]
	v_pk_mul_f32 v[168:169], v[44:45], v[166:167]
	v_pk_mul_f32 v[166:167], v[150:151], s[30:31] op_sel_hi:[1,0]
	v_pk_mul_f32 v[170:171], v[154:155], s[30:31] op_sel_hi:[1,0]
	s_mov_b64 s[84:85], 0
	v_pk_mul_f32 v[160:161], v[42:43], v[160:161]
	v_pk_mul_f32 v[170:171], v[40:41], v[170:171]
	v_pk_mul_f32 v[172:173], v[38:39], v[166:167]
	v_cvt_pk_bf16_f32 v166, v160, v161
	v_cvt_pk_bf16_f32 v167, v168, v169
	s_nop 0
	v_cvt_pk_bf16_f32 v168, v172, v173
	v_cvt_pk_bf16_f32 v169, v170, v171
	global_store_dwordx4 v[146:147], v[166:169], off
.LBB0_897:
	v_lshl_add_u64 v[158:159], v[158:159], 0, s[82:83]
	s_andn2_b64 vcc, exec, s[84:85]
	v_lshl_add_u64 v[4:5], v[158:159], 0, v[4:5]
	s_cbranch_vccnz .LBB0_899
	s_nop 0
	s_waitcnt vmcnt(1)
	v_mov_b32_e32 v158, v204
	v_mov_b32_e32 v159, v205
	v_cvt_f32_ubyte0_e32 v3, v158
	v_cvt_f32_ubyte1_e32 v161, v158
	v_cvt_f32_ubyte2_e32 v166, v158
	v_cvt_f32_ubyte3_e32 v167, v158
	v_cvt_f32_ubyte0_e32 v160, v159
	v_cvt_f32_ubyte1_e32 v168, v159
	v_cvt_f32_ubyte2_e32 v169, v159
	v_cvt_f32_ubyte3_e32 v170, v159
	v_rcp_iflag_f32_e32 v158, v3
	v_rcp_iflag_f32_e32 v160, v160
	v_rcp_iflag_f32_e32 v159, v161
	v_rcp_iflag_f32_e32 v161, v168
	v_rcp_iflag_f32_e32 v166, v166
	v_rcp_iflag_f32_e32 v167, v167
	v_rcp_iflag_f32_e32 v168, v169
	v_rcp_iflag_f32_e32 v169, v170
	v_pk_mul_f32 v[152:153], v[158:159], v[152:153]
	v_pk_mul_f32 v[156:157], v[166:167], v[156:157]
	v_pk_mul_f32 v[150:151], v[160:161], v[150:151]
	v_pk_mul_f32 v[154:155], v[168:169], v[154:155]
	v_pk_mul_f32 v[44:45], v[44:45], v[156:157]
	v_pk_mul_f32 v[42:43], v[42:43], v[152:153]
	v_pk_mul_f32 v[40:41], v[40:41], v[154:155]
	v_pk_mul_f32 v[38:39], v[38:39], v[150:151]
.LBB0_899:
	s_nop 0
	s_and_b64 vcc, exec, s[0:1]
	s_mov_b64 s[82:83], -1
	s_waitcnt vmcnt(2)
	v_mov_b32_e32 v156, v188
	v_mov_b32_e32 v157, v189
	v_cvt_f32_ubyte1_e32 v151, v156
	v_cvt_f32_ubyte0_e32 v150, v156
	v_cvt_f32_ubyte3_e32 v155, v156
	v_cvt_f32_ubyte2_e32 v154, v156
	v_cvt_f32_ubyte1_e32 v149, v157
	v_cvt_f32_ubyte0_e32 v148, v157
	v_cvt_f32_ubyte3_e32 v153, v157
	v_cvt_f32_ubyte2_e32 v152, v157
	s_cbranch_vccz .LBB0_902
	s_andn2_b64 vcc, exec, s[82:83]
	s_cbranch_vccz .LBB0_903

;     __device__ __forceinline__ bool operator()(f32x4 (&acc)[2][2][4][2], const Unit& u, int wr, int wc, int fr, int fq) const {
;     ...
;                     if (u.z < 2) { f32x4 h0, h1; unpack8_u8(*(const u32x2*)(G8 + (size_t)row * (NIN - C_G) + gn * DM + col), h0, h1);
; #pragma unroll
;                         for (int j = 0; j < 4; ++j) { g0[j] *= __builtin_amdgcn_rcpf(h0[j]); g1[j] *= __builtin_amdgcn_rcpf(h1[j]); }
;                         acc[ai][bj][m][0] *= g0; acc[ai][bj][m][1] *= g1;
.LBB0_903:
	s_nop 0
	s_waitcnt vmcnt(0)
	v_mov_b32_e32 v4, v206
	v_mov_b32_e32 v5, v207
	v_cvt_f32_ubyte0_e32 v3, v4
	v_cvt_f32_ubyte1_e32 v147, v4
	v_cvt_f32_ubyte2_e32 v156, v4
	v_cvt_f32_ubyte3_e32 v157, v4
	v_cvt_f32_ubyte0_e32 v146, v5
	v_cvt_f32_ubyte1_e32 v158, v5
	v_cvt_f32_ubyte2_e32 v159, v5
	v_cvt_f32_ubyte3_e32 v160, v5
	v_rcp_iflag_f32_e32 v4, v3
	v_rcp_iflag_f32_e32 v146, v146
	v_rcp_iflag_f32_e32 v5, v147
	v_rcp_iflag_f32_e32 v147, v158
	v_rcp_iflag_f32_e32 v156, v156
	v_rcp_iflag_f32_e32 v157, v157
	v_rcp_iflag_f32_e32 v158, v159
	v_rcp_iflag_f32_e32 v159, v160
	v_pk_mul_f32 v[4:5], v[4:5], v[150:151]
	v_pk_mul_f32 v[150:151], v[156:157], v[154:155]
	v_pk_mul_f32 v[146:147], v[146:147], v[148:149]
	v_pk_mul_f32 v[148:149], v[158:159], v[152:153]
	v_pk_mul_f32 v[12:13], v[12:13], v[150:151]
	v_pk_mul_f32 v[10:11], v[10:11], v[4:5]
	v_pk_mul_f32 v[8:9], v[8:9], v[148:149]
	v_pk_mul_f32 v[6:7], v[6:7], v[146:147]
	s_andn2_b64 vcc, exec, s[80:81]
	s_mov_b64 s[80:81], -1
	s_cbranch_vccnz .LBB0_831

; __device__ __forceinline__ u32x4 pack8(f32x4 v0, f32x4 v1) { u32x4 w; w.x = cvt_pk_bf16(v0[0], v0[1]); w.y = cvt_pk_bf16(v0[2], v0[3]); w.z = cvt_pk_bf16(v1[0], v1[1]); w.w = cvt_pk_bf16(v1[2], v1[3]); return w; }
; template <class T> __device__ __forceinline__ void est(T* p, T v) { if constexpr (MK_EPI_NT != 0) __builtin_nontemporal_store(v, p); else *p = v; }
;     __device__ __forceinline__ bool operator()(f32x4 (&acc)[2][2][4][2], const Unit& u, int wr, int wc, int fr, int fq) const {
;         const int row0 = u.pm * 256 + wr * 64 + fr, col0 = u.pn * 256 + wc * 32 + 8 * fq;
;         const int gc = u.z == 0 ? 0 : (u.z == 1 ? 2 : 1), gn = u.z == 0 ? 2 : 1;
; #pragma unroll
;         for (int ai = 0; ai < 2; ++ai)
; #pragma unroll
;             for (int m = 0; m < 4; ++m) { const int row = row0 + ai * 128 + m * 16;
; #pragma unroll
;                 for (int bj = 0; bj < 2; ++bj) { const int col = col0 + bj * 128; f32x4 g0, g1; unpack8_u8(*(const u32x2*)(G8 + (size_t)row * (NIN - C_G) + gc * DM + col), g0, g1);
;                     if (u.z < 2) { f32x4 h0, h1; unpack8_u8(*(const u32x2*)(G8 + (size_t)row * (NIN - C_G) + gn * DM + col), h0, h1);
; #pragma unroll
;                         for (int j = 0; j < 4; ++j) { g0[j] *= __builtin_amdgcn_rcpf(h0[j]); g1[j] *= __builtin_amdgcn_rcpf(h1[j]); }
;                         acc[ai][bj][m][0] *= g0; acc[ai][bj][m][1] *= g1;
;                     } else est((u32x4*)(mrgb + (size_t)row * DM + col), (u32x4)pack8(acc[ai][bj][m][0] * (g0 * (1.f / 255.f)), acc[ai][bj][m][1] * (g1 * (1.f / 255.f)))); } }
;         return u.z < 2;
.LBB0_1817:
	s_cmp_eq_u32 s40, 1
	s_cselect_b32 s0, s73, 0x800
	s_cmp_eq_u32 s40, 0
	v_lshl_add_u32 v146, s41, 8, v162
	v_mov_b64_e32 v[148:149], s[64:65]
	v_lshl_or_b32 v4, s8, 8, v164
	s_cselect_b32 s8, 0, s0
	v_mad_i64_i32 v[152:153], s[0:1], v146, s74, v[148:149]
	v_lshl_add_u64 v[148:149], v[152:153], 0, s[8:9]
	v_ashrrev_i32_e32 v5, 31, v4
	v_lshl_add_u64 v[150:151], v[148:149], 0, v[4:5]
	v_mov_b64_e32 v[208:209], v[150:151]
	s_movk_i32 s100, 0x800
	s_cmp_eq_u32 s40, 0
	s_cselect_b32 s100, 0x1000, s100
	s_mov_b32 s101, 0
	v_lshl_add_u64 v[210:211], v[152:153], 0, s[100:101]
	v_lshl_add_u64 v[210:211], v[210:211], 0, v[4:5]
	global_load_dwordx2 v[174:175], v[208:209], off
	global_load_dwordx2 v[190:191], v[210:211], off
	global_load_dwordx2 v[176:177], v[208:209], off offset:128
	global_load_dwordx2 v[192:193], v[210:211], off offset:128
	s_mov_b32 s100, 0x18000
	v_lshl_add_u64 v[212:213], v[208:209], 0, s[100:101]
	global_load_dwordx2 v[178:179], v[212:213], off
	s_mov_b32 s100, 0x18000
	v_lshl_add_u64 v[214:215], v[210:211], 0, s[100:101]
	global_load_dwordx2 v[196:197], v[214:215], off
	s_mov_b32 s100, 0x18000
	v_lshl_add_u64 v[212:213], v[208:209], 0, s[100:101]
	global_load_dwordx2 v[180:181], v[212:213], off offset:128
	s_mov_b32 s100, 0x18000
	v_lshl_add_u64 v[214:215], v[210:211], 0, s[100:101]
	global_load_dwordx2 v[198:199], v[214:215], off offset:128
	s_mov_b32 s100, 0x30000
	v_lshl_add_u64 v[212:213], v[208:209], 0, s[100:101]
	global_load_dwordx2 v[182:183], v[212:213], off
	s_mov_b32 s100, 0x30000
	v_lshl_add_u64 v[214:215], v[210:211], 0, s[100:101]
	global_load_dwordx2 v[200:201], v[214:215], off
	s_mov_b32 s100, 0x30000
	v_lshl_add_u64 v[212:213], v[208:209], 0, s[100:101]
	global_load_dwordx2 v[184:185], v[212:213], off offset:128
	s_mov_b32 s100, 0x30000
	v_lshl_add_u64 v[214:215], v[210:211], 0, s[100:101]
	global_load_dwordx2 v[202:203], v[214:215], off offset:128
	s_mov_b32 s100, 0x48000
	v_lshl_add_u64 v[212:213], v[208:209], 0, s[100:101]
	global_load_dwordx2 v[186:187], v[212:213], off
	s_mov_b32 s100, 0x48000
	v_lshl_add_u64 v[214:215], v[210:211], 0, s[100:101]
	global_load_dwordx2 v[204:205], v[214:215], off
	s_mov_b32 s100, 0x48000
	v_lshl_add_u64 v[212:213], v[208:209], 0, s[100:101]
	global_load_dwordx2 v[188:189], v[212:213], off offset:128
	s_mov_b32 s100, 0x48000
	v_lshl_add_u64 v[214:215], v[210:211], 0, s[100:101]
	global_load_dwordx2 v[206:207], v[214:215], off offset:128
	v_ashrrev_i32_e32 v147, 31, v146
	s_cselect_b32 s38, s73, 0x800
	v_lshlrev_b64 v[148:149], 12, v[146:147]
	s_cmp_gt_i32 s40, 1
	s_cselect_b64 s[40:41], -1, 0
	v_lshl_add_u64 v[148:149], s[60:61], 0, v[148:149]
	s_mov_b64 s[0:1], -1
	s_and_b64 vcc, exec, s[40:41]
	v_lshl_add_u64 v[148:149], v[4:5], 1, v[148:149]
	s_waitcnt vmcnt(15)
	v_mov_b32_e32 v166, v174
	v_mov_b32_e32 v167, v175
	s_mov_b32 s100, 0xc0000
	v_lshl_add_u64 v[212:213], v[208:209], 0, s[100:101]
	global_load_dwordx2 v[174:175], v[212:213], off
	v_cvt_f32_ubyte1_e32 v157, v166
	v_cvt_f32_ubyte0_e32 v156, v166
	v_cvt_f32_ubyte3_e32 v161, v166
	v_cvt_f32_ubyte2_e32 v160, v166
	v_cvt_f32_ubyte1_e32 v155, v167
	v_cvt_f32_ubyte0_e32 v154, v167
	v_cvt_f32_ubyte3_e32 v159, v167
	v_cvt_f32_ubyte2_e32 v158, v167
	s_cbranch_vccz .LBB0_1819
	v_pk_mul_f32 v[166:167], v[156:157], s[18:19] op_sel_hi:[1,0]
	v_pk_mul_f32 v[168:169], v[160:161], s[18:19] op_sel_hi:[1,0]
	v_pk_mul_f32 v[166:167], v[130:131], v[166:167]
	v_pk_mul_f32 v[168:169], v[132:133], v[168:169]
	v_pk_mul_f32 v[170:171], v[154:155], s[18:19] op_sel_hi:[1,0]
	v_pk_mul_f32 v[172:173], v[158:159], s[18:19] op_sel_hi:[1,0]
	v_pk_mul_f32 v[170:171], v[126:127], v[170:171]
	v_pk_mul_f32 v[172:173], v[128:129], v[172:173]
	v_cvt_pk_bf16_f32 v166, v166, v167
	v_cvt_pk_bf16_f32 v167, v168, v169
	v_cvt_pk_bf16_f32 v168, v170, v171
	s_mov_b64 s[0:1], 0
	v_cvt_pk_bf16_f32 v169, v172, v173
	global_store_dwordx4 v[148:149], v[166:169], off
.LBB0_1819:
	s_mov_b32 s39, s9
	v_lshl_add_u64 v[152:153], v[152:153], 0, s[38:39]
	s_andn2_b64 vcc, exec, s[0:1]
	v_lshl_add_u64 v[152:153], v[152:153], 0, v[4:5]
	s_cbranch_vccnz .LBB0_1821
	s_nop 0
	s_waitcnt vmcnt(15)
	v_mov_b32_e32 v166, v190
	v_mov_b32_e32 v167, v191
	v_cvt_f32_ubyte0_e32 v3, v166
	v_cvt_f32_ubyte1_e32 v147, v166
	v_cvt_f32_ubyte2_e32 v170, v166
	v_cvt_f32_ubyte3_e32 v171, v166
	v_cvt_f32_ubyte0_e32 v168, v167
	v_cvt_f32_ubyte1_e32 v169, v167
	v_cvt_f32_ubyte2_e32 v172, v167
	v_cvt_f32_ubyte3_e32 v173, v167
	v_rcp_iflag_f32_e32 v166, v3
	v_rcp_iflag_f32_e32 v168, v168
	v_rcp_iflag_f32_e32 v167, v147
	v_rcp_iflag_f32_e32 v169, v169
	v_rcp_iflag_f32_e32 v170, v170
	v_rcp_iflag_f32_e32 v171, v171
	v_rcp_iflag_f32_e32 v172, v172
	v_rcp_iflag_f32_e32 v173, v173
	v_pk_mul_f32 v[156:157], v[166:167], v[156:157]
	v_pk_mul_f32 v[160:161], v[170:171], v[160:161]
	v_pk_mul_f32 v[154:155], v[168:169], v[154:155]
	v_pk_mul_f32 v[158:159], v[172:173], v[158:159]
	v_pk_mul_f32 v[132:133], v[132:133], v[160:161]
	v_pk_mul_f32 v[130:131], v[130:131], v[156:157]
	v_pk_mul_f32 v[128:129], v[128:129], v[158:159]
	v_pk_mul_f32 v[126:127], v[126:127], v[154:155]
; __device__ __forceinline__ u32x4 pack8(f32x4 v0, f32x4 v1) { u32x4 w; w.x = cvt_pk_bf16(v0[0], v0[1]); w.y = cvt_pk_bf16(v0[2], v0[3]); w.z = cvt_pk_bf16(v1[0], v1[1]); w.w = cvt_pk_bf16(v1[2], v1[3]); return w; }
; template <class T> __device__ __forceinline__ void est(T* p, T v) { if constexpr (MK_EPI_NT != 0) __builtin_nontemporal_store(v, p); else *p = v; }
;     __device__ __forceinline__ bool operator()(f32x4 (&acc)[2][2][4][2], const Unit& u, int wr, int wc, int fr, int fq) const {
;     ...
;         for (int ai = 0; ai < 2; ++ai)
; #pragma unroll
;             for (int m = 0; m < 4; ++m) { const int row = row0 + ai * 128 + m * 16;
; #pragma unroll
;                 for (int bj = 0; bj < 2; ++bj) { const int col = col0 + bj * 128; f32x4 g0, g1; unpack8_u8(*(const u32x2*)(G8 + (size_t)row * (NIN - C_G) + gc * DM + col), g0, g1);
;                     if (u.z < 2) { f32x4 h0, h1; unpack8_u8(*(const u32x2*)(G8 + (size_t)row * (NIN - C_G) + gn * DM + col), h0, h1);
; #pragma unroll
;                         for (int j = 0; j < 4; ++j) { g0[j] *= __builtin_amdgcn_rcpf(h0[j]); g1[j] *= __builtin_amdgcn_rcpf(h1[j]); }
;                         acc[ai][bj][m][0] *= g0; acc[ai][bj][m][1] *= g1;
;                     } else est((u32x4*)(mrgb + (size_t)row * DM + col), (u32x4)pack8(acc[ai][bj][m][0] * (g0 * (1.f / 255.f)), acc[ai][bj][m][1] * (g1 * (1.f / 255.f)))); } }
.LBB0_1821:
	s_nop 0
	v_cndmask_b32_e64 v3, 0, 1, s[40:41]
	v_cmp_ne_u32_e64 s[0:1], 1, v3
	s_andn2_b64 vcc, exec, s[40:41]
	s_mov_b64 s[40:41], -1
	s_waitcnt vmcnt(14)
	v_mov_b32_e32 v160, v176
	v_mov_b32_e32 v161, v177
	s_mov_b32 s100, 0xc0000
	v_lshl_add_u64 v[212:213], v[208:209], 0, s[100:101]
	global_load_dwordx2 v[176:177], v[212:213], off offset:128
	s_mov_b32 s100, 0xc0000
	v_lshl_add_u64 v[214:215], v[210:211], 0, s[100:101]
	global_load_dwordx2 v[190:191], v[214:215], off
	v_cvt_f32_ubyte1_e32 v155, v160
	v_cvt_f32_ubyte0_e32 v154, v160
	v_cvt_f32_ubyte3_e32 v159, v160
	v_cvt_f32_ubyte2_e32 v158, v160
	v_cvt_f32_ubyte1_e32 v151, v161
	v_cvt_f32_ubyte0_e32 v150, v161
	v_cvt_f32_ubyte3_e32 v157, v161
	v_cvt_f32_ubyte2_e32 v156, v161
	s_cbranch_vccnz .LBB0_1823
	v_pk_mul_f32 v[166:167], v[158:159], s[18:19] op_sel_hi:[1,0]
	v_pk_mul_f32 v[160:161], v[154:155], s[18:19] op_sel_hi:[1,0]
	v_pk_mul_f32 v[168:169], v[100:101], v[166:167]
	v_pk_mul_f32 v[166:167], v[150:151], s[18:19] op_sel_hi:[1,0]
	v_pk_mul_f32 v[170:171], v[156:157], s[18:19] op_sel_hi:[1,0]
	s_mov_b64 s[40:41], 0
	v_pk_mul_f32 v[160:161], v[98:99], v[160:161]
	v_pk_mul_f32 v[170:171], v[96:97], v[170:171]
	v_pk_mul_f32 v[172:173], v[94:95], v[166:167]
	v_cvt_pk_bf16_f32 v166, v160, v161
	v_cvt_pk_bf16_f32 v167, v168, v169
	s_nop 0
	v_cvt_pk_bf16_f32 v168, v172, v173
	v_cvt_pk_bf16_f32 v169, v170, v171
	global_store_dwordx4 v[148:149], v[166:169], off offset:256
.LBB0_1823:
	s_andn2_b64 vcc, exec, s[40:41]
	s_cbranch_vccnz .LBB0_1825
	s_nop 0
	s_waitcnt vmcnt(15)
	v_mov_b32_e32 v148, v192
	v_mov_b32_e32 v149, v193
	v_cvt_f32_ubyte0_e32 v3, v148
	v_cvt_f32_ubyte1_e32 v147, v148
	v_cvt_f32_ubyte2_e32 v160, v148
	v_cvt_f32_ubyte3_e32 v161, v148
	v_cvt_f32_ubyte0_e32 v152, v149
	v_cvt_f32_ubyte1_e32 v153, v149
	v_cvt_f32_ubyte2_e32 v166, v149
	v_cvt_f32_ubyte3_e32 v167, v149
	v_rcp_iflag_f32_e32 v148, v3
	v_rcp_iflag_f32_e32 v152, v152
	v_rcp_iflag_f32_e32 v149, v147
	v_rcp_iflag_f32_e32 v153, v153
	v_rcp_iflag_f32_e32 v160, v160
	v_rcp_iflag_f32_e32 v161, v161
	v_rcp_iflag_f32_e32 v166, v166
	v_rcp_iflag_f32_e32 v167, v167
	v_pk_mul_f32 v[148:149], v[148:149], v[154:155]
	v_pk_mul_f32 v[154:155], v[160:161], v[158:159]
	v_pk_mul_f32 v[150:151], v[152:153], v[150:151]
	v_pk_mul_f32 v[152:153], v[166:167], v[156:157]
	v_pk_mul_f32 v[100:101], v[100:101], v[154:155]
	v_pk_mul_f32 v[98:99], v[98:99], v[148:149]
	v_pk_mul_f32 v[96:97], v[96:97], v[152:153]
	v_pk_mul_f32 v[94:95], v[94:95], v[150:151]
.LBB0_1825:
	v_or_b32_e32 v148, 16, v146
	v_mov_b64_e32 v[150:151], s[64:65]
	v_mad_i64_i32 v[152:153], s[40:41], v148, s74, v[150:151]
	v_lshl_add_u64 v[150:151], v[152:153], 0, s[8:9]
	v_lshl_add_u64 v[150:151], v[150:151], 0, v[4:5]
	s_nop 0
	v_ashrrev_i32_e32 v149, 31, v148
	v_lshlrev_b64 v[148:149], 12, v[148:149]
	v_lshl_add_u64 v[148:149], s[60:61], 0, v[148:149]
	s_mov_b64 s[40:41], -1
	s_and_b64 vcc, exec, s[0:1]
	v_lshl_add_u64 v[148:149], v[4:5], 1, v[148:149]
	s_waitcnt vmcnt(14)
	v_mov_b32_e32 v166, v178
	v_mov_b32_e32 v167, v179
	s_mov_b32 s100, 0xd8000
	v_lshl_add_u64 v[212:213], v[208:209], 0, s[100:101]
	global_load_dwordx2 v[178:179], v[212:213], off
	s_mov_b32 s100, 0xc0000
	v_lshl_add_u64 v[214:215], v[210:211], 0, s[100:101]
	global_load_dwordx2 v[192:193], v[214:215], off offset:128
	v_cvt_f32_ubyte1_e32 v157, v166
	v_cvt_f32_ubyte0_e32 v156, v166
	v_cvt_f32_ubyte3_e32 v161, v166
	v_cvt_f32_ubyte2_e32 v160, v166
	v_cvt_f32_ubyte1_e32 v155, v167
	v_cvt_f32_ubyte0_e32 v154, v167
	v_cvt_f32_ubyte3_e32 v159, v167
	v_cvt_f32_ubyte2_e32 v158, v167
	s_cbranch_vccnz .LBB0_1827
	v_pk_mul_f32 v[166:167], v[156:157], s[18:19] op_sel_hi:[1,0]
	v_pk_mul_f32 v[168:169], v[160:161], s[18:19] op_sel_hi:[1,0]
	v_pk_mul_f32 v[166:167], v[122:123], v[166:167]
	v_pk_mul_f32 v[168:169], v[124:125], v[168:169]
	v_pk_mul_f32 v[170:171], v[154:155], s[18:19] op_sel_hi:[1,0]
	v_pk_mul_f32 v[172:173], v[158:159], s[18:19] op_sel_hi:[1,0]
	s_mov_b64 s[40:41], 0
	v_pk_mul_f32 v[172:173], v[120:121], v[172:173]
	v_pk_mul_f32 v[170:171], v[118:119], v[170:171]
	v_cvt_pk_bf16_f32 v166, v166, v167
	v_cvt_pk_bf16_f32 v167, v168, v169
	s_nop 0
	v_cvt_pk_bf16_f32 v168, v170, v171
	v_cvt_pk_bf16_f32 v169, v172, v173
	global_store_dwordx4 v[148:149], v[166:169], off
.LBB0_1827:
	v_lshl_add_u64 v[152:153], v[152:153], 0, s[38:39]
	s_andn2_b64 vcc, exec, s[40:41]
	v_lshl_add_u64 v[152:153], v[152:153], 0, v[4:5]
	s_cbranch_vccnz .LBB0_1829
	s_nop 0
	s_waitcnt vmcnt(15)
	v_mov_b32_e32 v166, v196
	v_mov_b32_e32 v167, v197
	v_cvt_f32_ubyte0_e32 v3, v166
	v_cvt_f32_ubyte1_e32 v147, v166
	v_cvt_f32_ubyte2_e32 v170, v166
	v_cvt_f32_ubyte3_e32 v171, v166
	v_cvt_f32_ubyte0_e32 v168, v167
	v_cvt_f32_ubyte1_e32 v169, v167
	v_cvt_f32_ubyte2_e32 v172, v167
	v_cvt_f32_ubyte3_e32 v173, v167
	v_rcp_iflag_f32_e32 v166, v3
	v_rcp_iflag_f32_e32 v168, v168
	v_rcp_iflag_f32_e32 v167, v147
	v_rcp_iflag_f32_e32 v169, v169
	v_rcp_iflag_f32_e32 v170, v170
	v_rcp_iflag_f32_e32 v171, v171
	v_rcp_iflag_f32_e32 v172, v172
	v_rcp_iflag_f32_e32 v173, v173
	v_pk_mul_f32 v[156:157], v[166:167], v[156:157]
	v_pk_mul_f32 v[160:161], v[170:171], v[160:161]
	v_pk_mul_f32 v[154:155], v[168:169], v[154:155]
	v_pk_mul_f32 v[158:159], v[172:173], v[158:159]
	v_pk_mul_f32 v[124:125], v[124:125], v[160:161]
	v_pk_mul_f32 v[122:123], v[122:123], v[156:157]
	v_pk_mul_f32 v[120:121], v[120:121], v[158:159]
	v_pk_mul_f32 v[118:119], v[118:119], v[154:155]
; __device__ __forceinline__ u32x4 pack8(f32x4 v0, f32x4 v1) { u32x4 w; w.x = cvt_pk_bf16(v0[0], v0[1]); w.y = cvt_pk_bf16(v0[2], v0[3]); w.z = cvt_pk_bf16(v1[0], v1[1]); w.w = cvt_pk_bf16(v1[2], v1[3]); return w; }
; template <class T> __device__ __forceinline__ void est(T* p, T v) { if constexpr (MK_EPI_NT != 0) __builtin_nontemporal_store(v, p); else *p = v; }
;     __device__ __forceinline__ bool operator()(f32x4 (&acc)[2][2][4][2], const Unit& u, int wr, int wc, int fr, int fq) const {
;     ...
;         for (int ai = 0; ai < 2; ++ai)
; #pragma unroll
;             for (int m = 0; m < 4; ++m) { const int row = row0 + ai * 128 + m * 16;
; #pragma unroll
;                 for (int bj = 0; bj < 2; ++bj) { const int col = col0 + bj * 128; f32x4 g0, g1; unpack8_u8(*(const u32x2*)(G8 + (size_t)row * (NIN - C_G) + gc * DM + col), g0, g1);
;                     if (u.z < 2) { f32x4 h0, h1; unpack8_u8(*(const u32x2*)(G8 + (size_t)row * (NIN - C_G) + gn * DM + col), h0, h1);
; #pragma unroll
;                         for (int j = 0; j < 4; ++j) { g0[j] *= __builtin_amdgcn_rcpf(h0[j]); g1[j] *= __builtin_amdgcn_rcpf(h1[j]); }
;                         acc[ai][bj][m][0] *= g0; acc[ai][bj][m][1] *= g1;
;                     } else est((u32x4*)(mrgb + (size_t)row * DM + col), (u32x4)pack8(acc[ai][bj][m][0] * (g0 * (1.f / 255.f)), acc[ai][bj][m][1] * (g1 * (1.f / 255.f)))); } }
.LBB0_1829:
	s_nop 0
	s_and_b64 vcc, exec, s[0:1]
	s_mov_b64 s[40:41], -1
	s_waitcnt vmcnt(14)
	v_mov_b32_e32 v160, v180
	v_mov_b32_e32 v161, v181
	s_mov_b32 s100, 0xd8000
	v_lshl_add_u64 v[212:213], v[208:209], 0, s[100:101]
	global_load_dwordx2 v[180:181], v[212:213], off offset:128
	s_mov_b32 s100, 0xd8000
	v_lshl_add_u64 v[214:215], v[210:211], 0, s[100:101]
	global_load_dwordx2 v[196:197], v[214:215], off
	v_cvt_f32_ubyte1_e32 v155, v160
	v_cvt_f32_ubyte0_e32 v154, v160
	v_cvt_f32_ubyte3_e32 v159, v160
	v_cvt_f32_ubyte2_e32 v158, v160
	v_cvt_f32_ubyte1_e32 v151, v161
	v_cvt_f32_ubyte0_e32 v150, v161
	v_cvt_f32_ubyte3_e32 v157, v161
	v_cvt_f32_ubyte2_e32 v156, v161
	s_cbranch_vccnz .LBB0_1831
	v_pk_mul_f32 v[166:167], v[158:159], s[18:19] op_sel_hi:[1,0]
	v_pk_mul_f32 v[160:161], v[154:155], s[18:19] op_sel_hi:[1,0]
	v_pk_mul_f32 v[168:169], v[92:93], v[166:167]
	v_pk_mul_f32 v[166:167], v[150:151], s[18:19] op_sel_hi:[1,0]
	v_pk_mul_f32 v[170:171], v[156:157], s[18:19] op_sel_hi:[1,0]
	s_mov_b64 s[40:41], 0
	v_pk_mul_f32 v[160:161], v[90:91], v[160:161]
	v_pk_mul_f32 v[170:171], v[88:89], v[170:171]
	v_pk_mul_f32 v[172:173], v[86:87], v[166:167]
	v_cvt_pk_bf16_f32 v166, v160, v161
	v_cvt_pk_bf16_f32 v167, v168, v169
	s_nop 0
	v_cvt_pk_bf16_f32 v168, v172, v173
	v_cvt_pk_bf16_f32 v169, v170, v171
	global_store_dwordx4 v[148:149], v[166:169], off offset:256
.LBB0_1831:
	s_andn2_b64 vcc, exec, s[40:41]
	s_cbranch_vccnz .LBB0_1833
	s_nop 0
	s_waitcnt vmcnt(15)
	v_mov_b32_e32 v148, v198
	v_mov_b32_e32 v149, v199
	v_cvt_f32_ubyte0_e32 v3, v148
	v_cvt_f32_ubyte1_e32 v147, v148
	v_cvt_f32_ubyte2_e32 v160, v148
	v_cvt_f32_ubyte3_e32 v161, v148
	v_cvt_f32_ubyte0_e32 v152, v149
	v_cvt_f32_ubyte1_e32 v153, v149
	v_cvt_f32_ubyte2_e32 v166, v149
	v_cvt_f32_ubyte3_e32 v167, v149
	v_rcp_iflag_f32_e32 v148, v3
	v_rcp_iflag_f32_e32 v152, v152
	v_rcp_iflag_f32_e32 v149, v147
	v_rcp_iflag_f32_e32 v153, v153
	v_rcp_iflag_f32_e32 v160, v160
	v_rcp_iflag_f32_e32 v161, v161
	v_rcp_iflag_f32_e32 v166, v166
	v_rcp_iflag_f32_e32 v167, v167
	v_pk_mul_f32 v[148:149], v[148:149], v[154:155]
	v_pk_mul_f32 v[154:155], v[160:161], v[158:159]
	v_pk_mul_f32 v[150:151], v[152:153], v[150:151]
	v_pk_mul_f32 v[152:153], v[166:167], v[156:157]
	v_pk_mul_f32 v[92:93], v[92:93], v[154:155]
	v_pk_mul_f32 v[90:91], v[90:91], v[148:149]
	v_pk_mul_f32 v[88:89], v[88:89], v[152:153]
	v_pk_mul_f32 v[86:87], v[86:87], v[150:151]
.LBB0_1833:
	v_or_b32_e32 v148, 32, v146
	v_mov_b64_e32 v[150:151], s[64:65]
	v_mad_i64_i32 v[152:153], s[40:41], v148, s74, v[150:151]
	v_lshl_add_u64 v[150:151], v[152:153], 0, s[8:9]
	v_lshl_add_u64 v[150:151], v[150:151], 0, v[4:5]
	s_nop 0
	v_ashrrev_i32_e32 v149, 31, v148
	v_lshlrev_b64 v[148:149], 12, v[148:149]
	v_lshl_add_u64 v[148:149], s[60:61], 0, v[148:149]
	s_mov_b64 s[40:41], -1
	s_and_b64 vcc, exec, s[0:1]
	v_lshl_add_u64 v[148:149], v[4:5], 1, v[148:149]
	s_waitcnt vmcnt(14)
	v_mov_b32_e32 v166, v182
	v_mov_b32_e32 v167, v183
	s_mov_b32 s100, 0xf0000
	v_lshl_add_u64 v[212:213], v[208:209], 0, s[100:101]
	global_load_dwordx2 v[182:183], v[212:213], off
	s_mov_b32 s100, 0xd8000
	v_lshl_add_u64 v[214:215], v[210:211], 0, s[100:101]
	global_load_dwordx2 v[198:199], v[214:215], off offset:128
	v_cvt_f32_ubyte1_e32 v157, v166
	v_cvt_f32_ubyte0_e32 v156, v166
	v_cvt_f32_ubyte3_e32 v161, v166
	v_cvt_f32_ubyte2_e32 v160, v166
	v_cvt_f32_ubyte1_e32 v155, v167
	v_cvt_f32_ubyte0_e32 v154, v167
	v_cvt_f32_ubyte3_e32 v159, v167
	v_cvt_f32_ubyte2_e32 v158, v167
	s_cbranch_vccnz .LBB0_1835
	v_pk_mul_f32 v[166:167], v[156:157], s[18:19] op_sel_hi:[1,0]
	v_pk_mul_f32 v[168:169], v[160:161], s[18:19] op_sel_hi:[1,0]
	v_pk_mul_f32 v[166:167], v[114:115], v[166:167]
	v_pk_mul_f32 v[168:169], v[116:117], v[168:169]
	v_pk_mul_f32 v[170:171], v[154:155], s[18:19] op_sel_hi:[1,0]
	v_pk_mul_f32 v[172:173], v[158:159], s[18:19] op_sel_hi:[1,0]
	s_mov_b64 s[40:41], 0
	v_pk_mul_f32 v[172:173], v[112:113], v[172:173]
	v_pk_mul_f32 v[170:171], v[110:111], v[170:171]
	v_cvt_pk_bf16_f32 v166, v166, v167
	v_cvt_pk_bf16_f32 v167, v168, v169
	s_nop 0
	v_cvt_pk_bf16_f32 v168, v170, v171
	v_cvt_pk_bf16_f32 v169, v172, v173
	global_store_dwordx4 v[148:149], v[166:169], off
.LBB0_1835:
	v_lshl_add_u64 v[152:153], v[152:153], 0, s[38:39]
	s_andn2_b64 vcc, exec, s[40:41]
	v_lshl_add_u64 v[152:153], v[152:153], 0, v[4:5]
	s_cbranch_vccnz .LBB0_1837
	s_nop 0
	s_waitcnt vmcnt(15)
	v_mov_b32_e32 v166, v200
	v_mov_b32_e32 v167, v201
	v_cvt_f32_ubyte0_e32 v3, v166
	v_cvt_f32_ubyte1_e32 v147, v166
	v_cvt_f32_ubyte2_e32 v170, v166
	v_cvt_f32_ubyte3_e32 v171, v166
	v_cvt_f32_ubyte0_e32 v168, v167
	v_cvt_f32_ubyte1_e32 v169, v167
	v_cvt_f32_ubyte2_e32 v172, v167
	v_cvt_f32_ubyte3_e32 v173, v167
	v_rcp_iflag_f32_e32 v166, v3
	v_rcp_iflag_f32_e32 v168, v168
	v_rcp_iflag_f32_e32 v167, v147
	v_rcp_iflag_f32_e32 v169, v169
	v_rcp_iflag_f32_e32 v170, v170
	v_rcp_iflag_f32_e32 v171, v171
	v_rcp_iflag_f32_e32 v172, v172
	v_rcp_iflag_f32_e32 v173, v173
	v_pk_mul_f32 v[156:157], v[166:167], v[156:157]
	v_pk_mul_f32 v[160:161], v[170:171], v[160:161]
	v_pk_mul_f32 v[154:155], v[168:169], v[154:155]
	v_pk_mul_f32 v[158:159], v[172:173], v[158:159]
	v_pk_mul_f32 v[116:117], v[116:117], v[160:161]
	v_pk_mul_f32 v[114:115], v[114:115], v[156:157]
	v_pk_mul_f32 v[112:113], v[112:113], v[158:159]
	v_pk_mul_f32 v[110:111], v[110:111], v[154:155]
; __device__ __forceinline__ u32x4 pack8(f32x4 v0, f32x4 v1) { u32x4 w; w.x = cvt_pk_bf16(v0[0], v0[1]); w.y = cvt_pk_bf16(v0[2], v0[3]); w.z = cvt_pk_bf16(v1[0], v1[1]); w.w = cvt_pk_bf16(v1[2], v1[3]); return w; }
; template <class T> __device__ __forceinline__ void est(T* p, T v) { if constexpr (MK_EPI_NT != 0) __builtin_nontemporal_store(v, p); else *p = v; }
;     __device__ __forceinline__ bool operator()(f32x4 (&acc)[2][2][4][2], const Unit& u, int wr, int wc, int fr, int fq) const {
;     ...
;         for (int ai = 0; ai < 2; ++ai)
; #pragma unroll
;             for (int m = 0; m < 4; ++m) { const int row = row0 + ai * 128 + m * 16;
; #pragma unroll
;                 for (int bj = 0; bj < 2; ++bj) { const int col = col0 + bj * 128; f32x4 g0, g1; unpack8_u8(*(const u32x2*)(G8 + (size_t)row * (NIN - C_G) + gc * DM + col), g0, g1);
;                     if (u.z < 2) { f32x4 h0, h1; unpack8_u8(*(const u32x2*)(G8 + (size_t)row * (NIN - C_G) + gn * DM + col), h0, h1);
; #pragma unroll
;                         for (int j = 0; j < 4; ++j) { g0[j] *= __builtin_amdgcn_rcpf(h0[j]); g1[j] *= __builtin_amdgcn_rcpf(h1[j]); }
;                         acc[ai][bj][m][0] *= g0; acc[ai][bj][m][1] *= g1;
;                     } else est((u32x4*)(mrgb + (size_t)row * DM + col), (u32x4)pack8(acc[ai][bj][m][0] * (g0 * (1.f / 255.f)), acc[ai][bj][m][1] * (g1 * (1.f / 255.f)))); } }
.LBB0_1837:
	s_nop 0
	s_and_b64 vcc, exec, s[0:1]
	s_mov_b64 s[40:41], -1
	s_waitcnt vmcnt(14)
	v_mov_b32_e32 v160, v184
	v_mov_b32_e32 v161, v185
	s_mov_b32 s100, 0xf0000
	v_lshl_add_u64 v[212:213], v[208:209], 0, s[100:101]
	global_load_dwordx2 v[184:185], v[212:213], off offset:128
	s_mov_b32 s100, 0xf0000
	v_lshl_add_u64 v[214:215], v[210:211], 0, s[100:101]
	global_load_dwordx2 v[200:201], v[214:215], off
	v_cvt_f32_ubyte1_e32 v155, v160
	v_cvt_f32_ubyte0_e32 v154, v160
	v_cvt_f32_ubyte3_e32 v159, v160
	v_cvt_f32_ubyte2_e32 v158, v160
	v_cvt_f32_ubyte1_e32 v151, v161
	v_cvt_f32_ubyte0_e32 v150, v161
	v_cvt_f32_ubyte3_e32 v157, v161
	v_cvt_f32_ubyte2_e32 v156, v161
	s_cbranch_vccnz .LBB0_1839
	v_pk_mul_f32 v[166:167], v[158:159], s[18:19] op_sel_hi:[1,0]
	v_pk_mul_f32 v[160:161], v[154:155], s[18:19] op_sel_hi:[1,0]
	v_pk_mul_f32 v[168:169], v[84:85], v[166:167]
	v_pk_mul_f32 v[166:167], v[150:151], s[18:19] op_sel_hi:[1,0]
	v_pk_mul_f32 v[170:171], v[156:157], s[18:19] op_sel_hi:[1,0]
	s_mov_b64 s[40:41], 0
	v_pk_mul_f32 v[160:161], v[82:83], v[160:161]
	v_pk_mul_f32 v[170:171], v[80:81], v[170:171]
	v_pk_mul_f32 v[172:173], v[78:79], v[166:167]
	v_cvt_pk_bf16_f32 v166, v160, v161
	v_cvt_pk_bf16_f32 v167, v168, v169
	s_nop 0
	v_cvt_pk_bf16_f32 v168, v172, v173
	v_cvt_pk_bf16_f32 v169, v170, v171
	global_store_dwordx4 v[148:149], v[166:169], off offset:256
.LBB0_1839:
	s_andn2_b64 vcc, exec, s[40:41]
	s_cbranch_vccnz .LBB0_1841
	s_nop 0
	s_waitcnt vmcnt(15)
	v_mov_b32_e32 v148, v202
	v_mov_b32_e32 v149, v203
	v_cvt_f32_ubyte0_e32 v3, v148
	v_cvt_f32_ubyte1_e32 v147, v148
	v_cvt_f32_ubyte2_e32 v160, v148
	v_cvt_f32_ubyte3_e32 v161, v148
	v_cvt_f32_ubyte0_e32 v152, v149
	v_cvt_f32_ubyte1_e32 v153, v149
	v_cvt_f32_ubyte2_e32 v166, v149
	v_cvt_f32_ubyte3_e32 v167, v149
	v_rcp_iflag_f32_e32 v148, v3
	v_rcp_iflag_f32_e32 v152, v152
	v_rcp_iflag_f32_e32 v149, v147
	v_rcp_iflag_f32_e32 v153, v153
	v_rcp_iflag_f32_e32 v160, v160
	v_rcp_iflag_f32_e32 v161, v161
	v_rcp_iflag_f32_e32 v166, v166
	v_rcp_iflag_f32_e32 v167, v167
	v_pk_mul_f32 v[148:149], v[148:149], v[154:155]
	v_pk_mul_f32 v[154:155], v[160:161], v[158:159]
	v_pk_mul_f32 v[150:151], v[152:153], v[150:151]
	v_pk_mul_f32 v[152:153], v[166:167], v[156:157]
	v_pk_mul_f32 v[84:85], v[84:85], v[154:155]
	v_pk_mul_f32 v[82:83], v[82:83], v[148:149]
	v_pk_mul_f32 v[80:81], v[80:81], v[152:153]
	v_pk_mul_f32 v[78:79], v[78:79], v[150:151]
.LBB0_1841:
	v_or_b32_e32 v148, 48, v146
	v_mov_b64_e32 v[150:151], s[64:65]
	v_mad_i64_i32 v[152:153], s[40:41], v148, s74, v[150:151]
	v_lshl_add_u64 v[150:151], v[152:153], 0, s[8:9]
	v_lshl_add_u64 v[150:151], v[150:151], 0, v[4:5]
	s_nop 0
	v_ashrrev_i32_e32 v149, 31, v148
	v_lshlrev_b64 v[148:149], 12, v[148:149]
	v_lshl_add_u64 v[148:149], s[60:61], 0, v[148:149]
	s_mov_b64 s[40:41], -1
	s_and_b64 vcc, exec, s[0:1]
	v_lshl_add_u64 v[148:149], v[4:5], 1, v[148:149]
	s_waitcnt vmcnt(14)
	v_mov_b32_e32 v166, v186
	v_mov_b32_e32 v167, v187
	s_mov_b32 s100, 0x108000
	v_lshl_add_u64 v[212:213], v[208:209], 0, s[100:101]
	global_load_dwordx2 v[186:187], v[212:213], off
	s_mov_b32 s100, 0xf0000
	v_lshl_add_u64 v[214:215], v[210:211], 0, s[100:101]
	global_load_dwordx2 v[202:203], v[214:215], off offset:128
	v_cvt_f32_ubyte1_e32 v157, v166
	v_cvt_f32_ubyte0_e32 v156, v166
	v_cvt_f32_ubyte3_e32 v161, v166
	v_cvt_f32_ubyte2_e32 v160, v166
	v_cvt_f32_ubyte1_e32 v155, v167
	v_cvt_f32_ubyte0_e32 v154, v167
	v_cvt_f32_ubyte3_e32 v159, v167
	v_cvt_f32_ubyte2_e32 v158, v167
	s_cbranch_vccnz .LBB0_1843
	v_pk_mul_f32 v[166:167], v[156:157], s[18:19] op_sel_hi:[1,0]
	v_pk_mul_f32 v[168:169], v[160:161], s[18:19] op_sel_hi:[1,0]
	v_pk_mul_f32 v[166:167], v[106:107], v[166:167]
	v_pk_mul_f32 v[168:169], v[108:109], v[168:169]
	v_pk_mul_f32 v[170:171], v[154:155], s[18:19] op_sel_hi:[1,0]
	v_pk_mul_f32 v[172:173], v[158:159], s[18:19] op_sel_hi:[1,0]
	s_mov_b64 s[40:41], 0
	v_pk_mul_f32 v[172:173], v[104:105], v[172:173]
	v_pk_mul_f32 v[170:171], v[102:103], v[170:171]
	v_cvt_pk_bf16_f32 v166, v166, v167
	v_cvt_pk_bf16_f32 v167, v168, v169
	s_nop 0
	v_cvt_pk_bf16_f32 v168, v170, v171
	v_cvt_pk_bf16_f32 v169, v172, v173
	global_store_dwordx4 v[148:149], v[166:169], off
.LBB0_1843:
	v_lshl_add_u64 v[152:153], v[152:153], 0, s[38:39]
	s_andn2_b64 vcc, exec, s[40:41]
	v_lshl_add_u64 v[152:153], v[152:153], 0, v[4:5]
	s_cbranch_vccnz .LBB0_1845
	s_nop 0
	s_waitcnt vmcnt(15)
	v_mov_b32_e32 v166, v204
	v_mov_b32_e32 v167, v205
	v_cvt_f32_ubyte0_e32 v3, v166
	v_cvt_f32_ubyte1_e32 v147, v166
	v_cvt_f32_ubyte2_e32 v170, v166
	v_cvt_f32_ubyte3_e32 v171, v166
	v_cvt_f32_ubyte0_e32 v168, v167
	v_cvt_f32_ubyte1_e32 v169, v167
	v_cvt_f32_ubyte2_e32 v172, v167
	v_cvt_f32_ubyte3_e32 v173, v167
	v_rcp_iflag_f32_e32 v166, v3
	v_rcp_iflag_f32_e32 v168, v168
	v_rcp_iflag_f32_e32 v167, v147
	v_rcp_iflag_f32_e32 v169, v169
	v_rcp_iflag_f32_e32 v170, v170
	v_rcp_iflag_f32_e32 v171, v171
	v_rcp_iflag_f32_e32 v172, v172
	v_rcp_iflag_f32_e32 v173, v173
	v_pk_mul_f32 v[156:157], v[166:167], v[156:157]
	v_pk_mul_f32 v[160:161], v[170:171], v[160:161]
	v_pk_mul_f32 v[154:155], v[168:169], v[154:155]
	v_pk_mul_f32 v[158:159], v[172:173], v[158:159]
	v_pk_mul_f32 v[108:109], v[108:109], v[160:161]
	v_pk_mul_f32 v[106:107], v[106:107], v[156:157]
	v_pk_mul_f32 v[104:105], v[104:105], v[158:159]
	v_pk_mul_f32 v[102:103], v[102:103], v[154:155]
; __device__ __forceinline__ u32x4 pack8(f32x4 v0, f32x4 v1) { u32x4 w; w.x = cvt_pk_bf16(v0[0], v0[1]); w.y = cvt_pk_bf16(v0[2], v0[3]); w.z = cvt_pk_bf16(v1[0], v1[1]); w.w = cvt_pk_bf16(v1[2], v1[3]); return w; }
; template <class T> __device__ __forceinline__ void est(T* p, T v) { if constexpr (MK_EPI_NT != 0) __builtin_nontemporal_store(v, p); else *p = v; }
;     __device__ __forceinline__ bool operator()(f32x4 (&acc)[2][2][4][2], const Unit& u, int wr, int wc, int fr, int fq) const {
;     ...
;         for (int ai = 0; ai < 2; ++ai)
; #pragma unroll
;             for (int m = 0; m < 4; ++m) { const int row = row0 + ai * 128 + m * 16;
; #pragma unroll
;                 for (int bj = 0; bj < 2; ++bj) { const int col = col0 + bj * 128; f32x4 g0, g1; unpack8_u8(*(const u32x2*)(G8 + (size_t)row * (NIN - C_G) + gc * DM + col), g0, g1);
;                     if (u.z < 2) { f32x4 h0, h1; unpack8_u8(*(const u32x2*)(G8 + (size_t)row * (NIN - C_G) + gn * DM + col), h0, h1);
; #pragma unroll
;                         for (int j = 0; j < 4; ++j) { g0[j] *= __builtin_amdgcn_rcpf(h0[j]); g1[j] *= __builtin_amdgcn_rcpf(h1[j]); }
;                         acc[ai][bj][m][0] *= g0; acc[ai][bj][m][1] *= g1;
;                     } else est((u32x4*)(mrgb + (size_t)row * DM + col), (u32x4)pack8(acc[ai][bj][m][0] * (g0 * (1.f / 255.f)), acc[ai][bj][m][1] * (g1 * (1.f / 255.f)))); } }
.LBB0_1845:
	s_nop 0
	s_and_b64 vcc, exec, s[0:1]
	s_mov_b64 s[40:41], -1
	s_waitcnt vmcnt(14)
	v_mov_b32_e32 v160, v188
	v_mov_b32_e32 v161, v189
	s_mov_b32 s100, 0x108000
	v_lshl_add_u64 v[212:213], v[208:209], 0, s[100:101]
	global_load_dwordx2 v[188:189], v[212:213], off offset:128
	s_mov_b32 s100, 0x108000
	v_lshl_add_u64 v[214:215], v[210:211], 0, s[100:101]
	global_load_dwordx2 v[204:205], v[214:215], off
	v_cvt_f32_ubyte1_e32 v155, v160
	v_cvt_f32_ubyte0_e32 v154, v160
	v_cvt_f32_ubyte3_e32 v159, v160
	v_cvt_f32_ubyte2_e32 v158, v160
	v_cvt_f32_ubyte1_e32 v151, v161
	v_cvt_f32_ubyte0_e32 v150, v161
	v_cvt_f32_ubyte3_e32 v157, v161
	v_cvt_f32_ubyte2_e32 v156, v161
	s_cbranch_vccnz .LBB0_1847
	v_pk_mul_f32 v[166:167], v[158:159], s[18:19] op_sel_hi:[1,0]
	v_pk_mul_f32 v[160:161], v[154:155], s[18:19] op_sel_hi:[1,0]
	v_pk_mul_f32 v[168:169], v[76:77], v[166:167]
	v_pk_mul_f32 v[166:167], v[150:151], s[18:19] op_sel_hi:[1,0]
	v_pk_mul_f32 v[170:171], v[156:157], s[18:19] op_sel_hi:[1,0]
	s_mov_b64 s[40:41], 0
	v_pk_mul_f32 v[160:161], v[74:75], v[160:161]
	v_pk_mul_f32 v[170:171], v[72:73], v[170:171]
	v_pk_mul_f32 v[172:173], v[70:71], v[166:167]
	v_cvt_pk_bf16_f32 v166, v160, v161
	v_cvt_pk_bf16_f32 v167, v168, v169
	s_nop 0
	v_cvt_pk_bf16_f32 v168, v172, v173
	v_cvt_pk_bf16_f32 v169, v170, v171
	global_store_dwordx4 v[148:149], v[166:169], off offset:256
.LBB0_1847:
	s_andn2_b64 vcc, exec, s[40:41]
	s_cbranch_vccnz .LBB0_1849
	s_nop 0
	s_waitcnt vmcnt(15)
	v_mov_b32_e32 v148, v206
	v_mov_b32_e32 v149, v207
	v_cvt_f32_ubyte0_e32 v3, v148
	v_cvt_f32_ubyte1_e32 v147, v148
	v_cvt_f32_ubyte2_e32 v160, v148
	v_cvt_f32_ubyte3_e32 v161, v148
	v_cvt_f32_ubyte0_e32 v152, v149
	v_cvt_f32_ubyte1_e32 v153, v149
	v_cvt_f32_ubyte2_e32 v166, v149
	v_cvt_f32_ubyte3_e32 v167, v149
	v_rcp_iflag_f32_e32 v148, v3
	v_rcp_iflag_f32_e32 v152, v152
	v_rcp_iflag_f32_e32 v149, v147
	v_rcp_iflag_f32_e32 v153, v153
	v_rcp_iflag_f32_e32 v160, v160
	v_rcp_iflag_f32_e32 v161, v161
	v_rcp_iflag_f32_e32 v166, v166
	v_rcp_iflag_f32_e32 v167, v167
	v_pk_mul_f32 v[148:149], v[148:149], v[154:155]
	v_pk_mul_f32 v[154:155], v[160:161], v[158:159]
	v_pk_mul_f32 v[150:151], v[152:153], v[150:151]
	v_pk_mul_f32 v[152:153], v[166:167], v[156:157]
	v_pk_mul_f32 v[76:77], v[76:77], v[154:155]
	v_pk_mul_f32 v[74:75], v[74:75], v[148:149]
	v_pk_mul_f32 v[72:73], v[72:73], v[152:153]
	v_pk_mul_f32 v[70:71], v[70:71], v[150:151]
.LBB0_1849:
	v_add_u32_e32 v148, 0x80, v146
	v_mov_b64_e32 v[150:151], s[64:65]
	v_mad_i64_i32 v[152:153], s[40:41], v148, s74, v[150:151]
	v_lshl_add_u64 v[150:151], v[152:153], 0, s[8:9]
	v_lshl_add_u64 v[150:151], v[150:151], 0, v[4:5]
	s_nop 0
	v_ashrrev_i32_e32 v149, 31, v148
	v_lshlrev_b64 v[148:149], 12, v[148:149]
	v_lshl_add_u64 v[148:149], s[60:61], 0, v[148:149]
	s_mov_b64 s[40:41], -1
	s_and_b64 vcc, exec, s[0:1]
	v_lshl_add_u64 v[148:149], v[4:5], 1, v[148:149]
	s_waitcnt vmcnt(14)
	v_mov_b32_e32 v166, v174
	v_mov_b32_e32 v167, v175
	s_mov_b32 s100, 0x108000
	v_lshl_add_u64 v[214:215], v[210:211], 0, s[100:101]
	global_load_dwordx2 v[206:207], v[214:215], off offset:128
	v_cvt_f32_ubyte1_e32 v157, v166
	v_cvt_f32_ubyte0_e32 v156, v166
	v_cvt_f32_ubyte3_e32 v161, v166
	v_cvt_f32_ubyte2_e32 v160, v166
	v_cvt_f32_ubyte1_e32 v155, v167
	v_cvt_f32_ubyte0_e32 v154, v167
	v_cvt_f32_ubyte3_e32 v159, v167
	v_cvt_f32_ubyte2_e32 v158, v167
	s_cbranch_vccnz .LBB0_1851
	v_pk_mul_f32 v[166:167], v[156:157], s[18:19] op_sel_hi:[1,0]
	v_pk_mul_f32 v[168:169], v[160:161], s[18:19] op_sel_hi:[1,0]
	v_pk_mul_f32 v[166:167], v[66:67], v[166:167]
	v_pk_mul_f32 v[168:169], v[68:69], v[168:169]
	v_pk_mul_f32 v[170:171], v[154:155], s[18:19] op_sel_hi:[1,0]
	v_pk_mul_f32 v[172:173], v[158:159], s[18:19] op_sel_hi:[1,0]
	s_mov_b64 s[40:41], 0
	v_pk_mul_f32 v[172:173], v[64:65], v[172:173]
	v_pk_mul_f32 v[170:171], v[62:63], v[170:171]
	v_cvt_pk_bf16_f32 v166, v166, v167
	v_cvt_pk_bf16_f32 v167, v168, v169
	s_nop 0
	v_cvt_pk_bf16_f32 v168, v170, v171
	v_cvt_pk_bf16_f32 v169, v172, v173
	global_store_dwordx4 v[148:149], v[166:169], off
.LBB0_1851:
	v_lshl_add_u64 v[152:153], v[152:153], 0, s[38:39]
	s_andn2_b64 vcc, exec, s[40:41]
	v_lshl_add_u64 v[152:153], v[152:153], 0, v[4:5]
	s_cbranch_vccnz .LBB0_1853
	s_nop 0
	s_waitcnt vmcnt(13)
	v_mov_b32_e32 v166, v190
	v_mov_b32_e32 v167, v191
	v_cvt_f32_ubyte0_e32 v3, v166
	v_cvt_f32_ubyte1_e32 v147, v166
	v_cvt_f32_ubyte2_e32 v170, v166
	v_cvt_f32_ubyte3_e32 v171, v166
	v_cvt_f32_ubyte0_e32 v168, v167
	v_cvt_f32_ubyte1_e32 v169, v167
	v_cvt_f32_ubyte2_e32 v172, v167
	v_cvt_f32_ubyte3_e32 v173, v167
	v_rcp_iflag_f32_e32 v166, v3
	v_rcp_iflag_f32_e32 v168, v168
	v_rcp_iflag_f32_e32 v167, v147
	v_rcp_iflag_f32_e32 v169, v169
	v_rcp_iflag_f32_e32 v170, v170
	v_rcp_iflag_f32_e32 v171, v171
	v_rcp_iflag_f32_e32 v172, v172
	v_rcp_iflag_f32_e32 v173, v173
	v_pk_mul_f32 v[156:157], v[166:167], v[156:157]
	v_pk_mul_f32 v[160:161], v[170:171], v[160:161]
	v_pk_mul_f32 v[154:155], v[168:169], v[154:155]
	v_pk_mul_f32 v[158:159], v[172:173], v[158:159]
	v_pk_mul_f32 v[68:69], v[68:69], v[160:161]
	v_pk_mul_f32 v[66:67], v[66:67], v[156:157]
	v_pk_mul_f32 v[64:65], v[64:65], v[158:159]
	v_pk_mul_f32 v[62:63], v[62:63], v[154:155]
; __device__ __forceinline__ u32x4 pack8(f32x4 v0, f32x4 v1) { u32x4 w; w.x = cvt_pk_bf16(v0[0], v0[1]); w.y = cvt_pk_bf16(v0[2], v0[3]); w.z = cvt_pk_bf16(v1[0], v1[1]); w.w = cvt_pk_bf16(v1[2], v1[3]); return w; }
; template <class T> __device__ __forceinline__ void est(T* p, T v) { if constexpr (MK_EPI_NT != 0) __builtin_nontemporal_store(v, p); else *p = v; }
;     __device__ __forceinline__ bool operator()(f32x4 (&acc)[2][2][4][2], const Unit& u, int wr, int wc, int fr, int fq) const {
;     ...
;         for (int ai = 0; ai < 2; ++ai)
; #pragma unroll
;             for (int m = 0; m < 4; ++m) { const int row = row0 + ai * 128 + m * 16;
; #pragma unroll
;                 for (int bj = 0; bj < 2; ++bj) { const int col = col0 + bj * 128; f32x4 g0, g1; unpack8_u8(*(const u32x2*)(G8 + (size_t)row * (NIN - C_G) + gc * DM + col), g0, g1);
;                     if (u.z < 2) { f32x4 h0, h1; unpack8_u8(*(const u32x2*)(G8 + (size_t)row * (NIN - C_G) + gn * DM + col), h0, h1);
; #pragma unroll
;                         for (int j = 0; j < 4; ++j) { g0[j] *= __builtin_amdgcn_rcpf(h0[j]); g1[j] *= __builtin_amdgcn_rcpf(h1[j]); }
;                         acc[ai][bj][m][0] *= g0; acc[ai][bj][m][1] *= g1;
;                     } else est((u32x4*)(mrgb + (size_t)row * DM + col), (u32x4)pack8(acc[ai][bj][m][0] * (g0 * (1.f / 255.f)), acc[ai][bj][m][1] * (g1 * (1.f / 255.f)))); } }
.LBB0_1853:
	s_nop 0
	s_and_b64 vcc, exec, s[0:1]
	s_mov_b64 s[40:41], -1
	s_waitcnt vmcnt(14)
	v_mov_b32_e32 v160, v176
	v_mov_b32_e32 v161, v177
	v_cvt_f32_ubyte1_e32 v155, v160
	v_cvt_f32_ubyte0_e32 v154, v160
	v_cvt_f32_ubyte3_e32 v159, v160
	v_cvt_f32_ubyte2_e32 v158, v160
	v_cvt_f32_ubyte1_e32 v151, v161
	v_cvt_f32_ubyte0_e32 v150, v161
	v_cvt_f32_ubyte3_e32 v157, v161
	v_cvt_f32_ubyte2_e32 v156, v161
	s_cbranch_vccnz .LBB0_1855
	v_pk_mul_f32 v[166:167], v[158:159], s[18:19] op_sel_hi:[1,0]
	v_pk_mul_f32 v[160:161], v[154:155], s[18:19] op_sel_hi:[1,0]
	v_pk_mul_f32 v[168:169], v[36:37], v[166:167]
	v_pk_mul_f32 v[166:167], v[150:151], s[18:19] op_sel_hi:[1,0]
	v_pk_mul_f32 v[170:171], v[156:157], s[18:19] op_sel_hi:[1,0]
	s_mov_b64 s[40:41], 0
	v_pk_mul_f32 v[160:161], v[34:35], v[160:161]
	v_pk_mul_f32 v[170:171], v[32:33], v[170:171]
	v_pk_mul_f32 v[172:173], v[30:31], v[166:167]
	v_cvt_pk_bf16_f32 v166, v160, v161
	v_cvt_pk_bf16_f32 v167, v168, v169
	s_nop 0
	v_cvt_pk_bf16_f32 v168, v172, v173
	v_cvt_pk_bf16_f32 v169, v170, v171
	global_store_dwordx4 v[148:149], v[166:169], off offset:256
.LBB0_1855:
	s_andn2_b64 vcc, exec, s[40:41]
	s_cbranch_vccnz .LBB0_1857
	s_nop 0
	s_waitcnt vmcnt(11)
	v_mov_b32_e32 v148, v192
	v_mov_b32_e32 v149, v193
	v_cvt_f32_ubyte0_e32 v3, v148
	v_cvt_f32_ubyte1_e32 v147, v148
	v_cvt_f32_ubyte2_e32 v160, v148
	v_cvt_f32_ubyte3_e32 v161, v148
	v_cvt_f32_ubyte0_e32 v152, v149
	v_cvt_f32_ubyte1_e32 v153, v149
	v_cvt_f32_ubyte2_e32 v166, v149
	v_cvt_f32_ubyte3_e32 v167, v149
	v_rcp_iflag_f32_e32 v148, v3
	v_rcp_iflag_f32_e32 v152, v152
	v_rcp_iflag_f32_e32 v149, v147
	v_rcp_iflag_f32_e32 v153, v153
	v_rcp_iflag_f32_e32 v160, v160
	v_rcp_iflag_f32_e32 v161, v161
	v_rcp_iflag_f32_e32 v166, v166
	v_rcp_iflag_f32_e32 v167, v167
	v_pk_mul_f32 v[148:149], v[148:149], v[154:155]
	v_pk_mul_f32 v[154:155], v[160:161], v[158:159]
	v_pk_mul_f32 v[150:151], v[152:153], v[150:151]
	v_pk_mul_f32 v[152:153], v[166:167], v[156:157]
	v_pk_mul_f32 v[36:37], v[36:37], v[154:155]
	v_pk_mul_f32 v[34:35], v[34:35], v[148:149]
	v_pk_mul_f32 v[32:33], v[32:33], v[152:153]
	v_pk_mul_f32 v[30:31], v[30:31], v[150:151]
.LBB0_1857:
	v_add_u32_e32 v148, 0x90, v146
	v_mov_b64_e32 v[150:151], s[64:65]
	v_mad_i64_i32 v[152:153], s[40:41], v148, s74, v[150:151]
	v_lshl_add_u64 v[150:151], v[152:153], 0, s[8:9]
	v_lshl_add_u64 v[150:151], v[150:151], 0, v[4:5]
	s_nop 0
	v_ashrrev_i32_e32 v149, 31, v148
	v_lshlrev_b64 v[148:149], 12, v[148:149]
	v_lshl_add_u64 v[148:149], s[60:61], 0, v[148:149]
	s_mov_b64 s[40:41], -1
	s_and_b64 vcc, exec, s[0:1]
	v_lshl_add_u64 v[148:149], v[4:5], 1, v[148:149]
	s_waitcnt vmcnt(12)
	v_mov_b32_e32 v166, v178
	v_mov_b32_e32 v167, v179
	v_cvt_f32_ubyte1_e32 v157, v166
	v_cvt_f32_ubyte0_e32 v156, v166
	v_cvt_f32_ubyte3_e32 v161, v166
	v_cvt_f32_ubyte2_e32 v160, v166
	v_cvt_f32_ubyte1_e32 v155, v167
	v_cvt_f32_ubyte0_e32 v154, v167
	v_cvt_f32_ubyte3_e32 v159, v167
	v_cvt_f32_ubyte2_e32 v158, v167
	s_cbranch_vccnz .LBB0_1859
	v_pk_mul_f32 v[166:167], v[156:157], s[18:19] op_sel_hi:[1,0]
	v_pk_mul_f32 v[168:169], v[160:161], s[18:19] op_sel_hi:[1,0]
	v_pk_mul_f32 v[166:167], v[58:59], v[166:167]
	v_pk_mul_f32 v[168:169], v[60:61], v[168:169]
	v_pk_mul_f32 v[170:171], v[154:155], s[18:19] op_sel_hi:[1,0]
	v_pk_mul_f32 v[172:173], v[158:159], s[18:19] op_sel_hi:[1,0]
	s_mov_b64 s[40:41], 0
	v_pk_mul_f32 v[172:173], v[56:57], v[172:173]
	v_pk_mul_f32 v[170:171], v[54:55], v[170:171]
	v_cvt_pk_bf16_f32 v166, v166, v167
	v_cvt_pk_bf16_f32 v167, v168, v169
	s_nop 0
	v_cvt_pk_bf16_f32 v168, v170, v171
	v_cvt_pk_bf16_f32 v169, v172, v173
	global_store_dwordx4 v[148:149], v[166:169], off
.LBB0_1859:
	v_lshl_add_u64 v[152:153], v[152:153], 0, s[38:39]
	s_andn2_b64 vcc, exec, s[40:41]
	v_lshl_add_u64 v[152:153], v[152:153], 0, v[4:5]
	s_cbranch_vccnz .LBB0_1861
	s_nop 0
	s_waitcnt vmcnt(9)
	v_mov_b32_e32 v166, v196
	v_mov_b32_e32 v167, v197
	v_cvt_f32_ubyte0_e32 v3, v166
	v_cvt_f32_ubyte1_e32 v147, v166
	v_cvt_f32_ubyte2_e32 v170, v166
	v_cvt_f32_ubyte3_e32 v171, v166
	v_cvt_f32_ubyte0_e32 v168, v167
	v_cvt_f32_ubyte1_e32 v169, v167
	v_cvt_f32_ubyte2_e32 v172, v167
	v_cvt_f32_ubyte3_e32 v173, v167
	v_rcp_iflag_f32_e32 v166, v3
	v_rcp_iflag_f32_e32 v168, v168
	v_rcp_iflag_f32_e32 v167, v147
	v_rcp_iflag_f32_e32 v169, v169
	v_rcp_iflag_f32_e32 v170, v170
	v_rcp_iflag_f32_e32 v171, v171
	v_rcp_iflag_f32_e32 v172, v172
	v_rcp_iflag_f32_e32 v173, v173
	v_pk_mul_f32 v[156:157], v[166:167], v[156:157]
	v_pk_mul_f32 v[160:161], v[170:171], v[160:161]
	v_pk_mul_f32 v[154:155], v[168:169], v[154:155]
	v_pk_mul_f32 v[158:159], v[172:173], v[158:159]
	v_pk_mul_f32 v[60:61], v[60:61], v[160:161]
	v_pk_mul_f32 v[58:59], v[58:59], v[156:157]
	v_pk_mul_f32 v[56:57], v[56:57], v[158:159]
	v_pk_mul_f32 v[54:55], v[54:55], v[154:155]
.LBB0_1861:
	s_nop 0
	s_and_b64 vcc, exec, s[0:1]
	s_mov_b64 s[40:41], -1
	s_waitcnt vmcnt(10)
	v_mov_b32_e32 v160, v180
	v_mov_b32_e32 v161, v181
	v_cvt_f32_ubyte1_e32 v155, v160
	v_cvt_f32_ubyte0_e32 v154, v160
	v_cvt_f32_ubyte3_e32 v159, v160
	v_cvt_f32_ubyte2_e32 v158, v160
	v_cvt_f32_ubyte1_e32 v151, v161
	v_cvt_f32_ubyte0_e32 v150, v161
	v_cvt_f32_ubyte3_e32 v157, v161
	v_cvt_f32_ubyte2_e32 v156, v161
	s_cbranch_vccnz .LBB0_1863
	v_pk_mul_f32 v[166:167], v[158:159], s[18:19] op_sel_hi:[1,0]
	v_pk_mul_f32 v[160:161], v[154:155], s[18:19] op_sel_hi:[1,0]
	v_pk_mul_f32 v[168:169], v[28:29], v[166:167]
	v_pk_mul_f32 v[166:167], v[150:151], s[18:19] op_sel_hi:[1,0]
	v_pk_mul_f32 v[170:171], v[156:157], s[18:19] op_sel_hi:[1,0]
	s_mov_b64 s[40:41], 0
	v_pk_mul_f32 v[160:161], v[26:27], v[160:161]
	v_pk_mul_f32 v[170:171], v[24:25], v[170:171]
	v_pk_mul_f32 v[172:173], v[22:23], v[166:167]
	v_cvt_pk_bf16_f32 v166, v160, v161
	v_cvt_pk_bf16_f32 v167, v168, v169
	s_nop 0
	v_cvt_pk_bf16_f32 v168, v172, v173
	v_cvt_pk_bf16_f32 v169, v170, v171
	global_store_dwordx4 v[148:149], v[166:169], off offset:256
; __device__ __forceinline__ u32x4 pack8(f32x4 v0, f32x4 v1) { u32x4 w; w.x = cvt_pk_bf16(v0[0], v0[1]); w.y = cvt_pk_bf16(v0[2], v0[3]); w.z = cvt_pk_bf16(v1[0], v1[1]); w.w = cvt_pk_bf16(v1[2], v1[3]); return w; }
; template <class T> __device__ __forceinline__ void est(T* p, T v) { if constexpr (MK_EPI_NT != 0) __builtin_nontemporal_store(v, p); else *p = v; }
;     __device__ __forceinline__ bool operator()(f32x4 (&acc)[2][2][4][2], const Unit& u, int wr, int wc, int fr, int fq) const {
;     ...
;         for (int ai = 0; ai < 2; ++ai)
; #pragma unroll
;             for (int m = 0; m < 4; ++m) { const int row = row0 + ai * 128 + m * 16;
; #pragma unroll
;                 for (int bj = 0; bj < 2; ++bj) { const int col = col0 + bj * 128; f32x4 g0, g1; unpack8_u8(*(const u32x2*)(G8 + (size_t)row * (NIN - C_G) + gc * DM + col), g0, g1);
;                     if (u.z < 2) { f32x4 h0, h1; unpack8_u8(*(const u32x2*)(G8 + (size_t)row * (NIN - C_G) + gn * DM + col), h0, h1);
; #pragma unroll
;                         for (int j = 0; j < 4; ++j) { g0[j] *= __builtin_amdgcn_rcpf(h0[j]); g1[j] *= __builtin_amdgcn_rcpf(h1[j]); }
;                         acc[ai][bj][m][0] *= g0; acc[ai][bj][m][1] *= g1;
;                     } else est((u32x4*)(mrgb + (size_t)row * DM + col), (u32x4)pack8(acc[ai][bj][m][0] * (g0 * (1.f / 255.f)), acc[ai][bj][m][1] * (g1 * (1.f / 255.f)))); } }
.LBB0_1863:
	s_andn2_b64 vcc, exec, s[40:41]
	s_cbranch_vccnz .LBB0_1865
	s_nop 0
	s_waitcnt vmcnt(7)
	v_mov_b32_e32 v148, v198
	v_mov_b32_e32 v149, v199
	v_cvt_f32_ubyte0_e32 v3, v148
	v_cvt_f32_ubyte1_e32 v147, v148
	v_cvt_f32_ubyte2_e32 v160, v148
	v_cvt_f32_ubyte3_e32 v161, v148
	v_cvt_f32_ubyte0_e32 v152, v149
	v_cvt_f32_ubyte1_e32 v153, v149
	v_cvt_f32_ubyte2_e32 v166, v149
	v_cvt_f32_ubyte3_e32 v167, v149
	v_rcp_iflag_f32_e32 v148, v3
	v_rcp_iflag_f32_e32 v152, v152
	v_rcp_iflag_f32_e32 v149, v147
	v_rcp_iflag_f32_e32 v153, v153
	v_rcp_iflag_f32_e32 v160, v160
	v_rcp_iflag_f32_e32 v161, v161
	v_rcp_iflag_f32_e32 v166, v166
	v_rcp_iflag_f32_e32 v167, v167
	v_pk_mul_f32 v[148:149], v[148:149], v[154:155]
	v_pk_mul_f32 v[154:155], v[160:161], v[158:159]
	v_pk_mul_f32 v[150:151], v[152:153], v[150:151]
	v_pk_mul_f32 v[152:153], v[166:167], v[156:157]
	v_pk_mul_f32 v[28:29], v[28:29], v[154:155]
	v_pk_mul_f32 v[26:27], v[26:27], v[148:149]
	v_pk_mul_f32 v[24:25], v[24:25], v[152:153]
	v_pk_mul_f32 v[22:23], v[22:23], v[150:151]
.LBB0_1865:
	v_add_u32_e32 v148, 0xa0, v146
	v_mov_b64_e32 v[150:151], s[64:65]
	v_mad_i64_i32 v[152:153], s[40:41], v148, s74, v[150:151]
	v_lshl_add_u64 v[150:151], v[152:153], 0, s[8:9]
	v_lshl_add_u64 v[150:151], v[150:151], 0, v[4:5]
	s_nop 0
	v_ashrrev_i32_e32 v149, 31, v148
	v_lshlrev_b64 v[148:149], 12, v[148:149]
	v_lshl_add_u64 v[148:149], s[60:61], 0, v[148:149]
	s_mov_b64 s[40:41], -1
	s_and_b64 vcc, exec, s[0:1]
	v_lshl_add_u64 v[148:149], v[4:5], 1, v[148:149]
	s_waitcnt vmcnt(8)
	v_mov_b32_e32 v166, v182
	v_mov_b32_e32 v167, v183
	v_cvt_f32_ubyte1_e32 v157, v166
	v_cvt_f32_ubyte0_e32 v156, v166
	v_cvt_f32_ubyte3_e32 v161, v166
	v_cvt_f32_ubyte2_e32 v160, v166
	v_cvt_f32_ubyte1_e32 v155, v167
	v_cvt_f32_ubyte0_e32 v154, v167
	v_cvt_f32_ubyte3_e32 v159, v167
	v_cvt_f32_ubyte2_e32 v158, v167
	s_cbranch_vccnz .LBB0_1867
	v_pk_mul_f32 v[166:167], v[156:157], s[18:19] op_sel_hi:[1,0]
	v_pk_mul_f32 v[168:169], v[160:161], s[18:19] op_sel_hi:[1,0]
	v_pk_mul_f32 v[166:167], v[50:51], v[166:167]
	v_pk_mul_f32 v[168:169], v[52:53], v[168:169]
	v_pk_mul_f32 v[170:171], v[154:155], s[18:19] op_sel_hi:[1,0]
	v_pk_mul_f32 v[172:173], v[158:159], s[18:19] op_sel_hi:[1,0]
	s_mov_b64 s[40:41], 0
	v_pk_mul_f32 v[172:173], v[48:49], v[172:173]
	v_pk_mul_f32 v[170:171], v[46:47], v[170:171]
	v_cvt_pk_bf16_f32 v166, v166, v167
	v_cvt_pk_bf16_f32 v167, v168, v169
	s_nop 0
	v_cvt_pk_bf16_f32 v168, v170, v171
	v_cvt_pk_bf16_f32 v169, v172, v173
	global_store_dwordx4 v[148:149], v[166:169], off
.LBB0_1867:
	v_lshl_add_u64 v[152:153], v[152:153], 0, s[38:39]
	s_andn2_b64 vcc, exec, s[40:41]
	v_lshl_add_u64 v[152:153], v[152:153], 0, v[4:5]
	s_cbranch_vccnz .LBB0_1869
	s_nop 0
	s_waitcnt vmcnt(5)
	v_mov_b32_e32 v166, v200
	v_mov_b32_e32 v167, v201
	v_cvt_f32_ubyte0_e32 v3, v166
	v_cvt_f32_ubyte1_e32 v147, v166
	v_cvt_f32_ubyte2_e32 v170, v166
	v_cvt_f32_ubyte3_e32 v171, v166
	v_cvt_f32_ubyte0_e32 v168, v167
	v_cvt_f32_ubyte1_e32 v169, v167
	v_cvt_f32_ubyte2_e32 v172, v167
	v_cvt_f32_ubyte3_e32 v173, v167
	v_rcp_iflag_f32_e32 v166, v3
	v_rcp_iflag_f32_e32 v168, v168
	v_rcp_iflag_f32_e32 v167, v147
	v_rcp_iflag_f32_e32 v169, v169
	v_rcp_iflag_f32_e32 v170, v170
	v_rcp_iflag_f32_e32 v171, v171
	v_rcp_iflag_f32_e32 v172, v172
	v_rcp_iflag_f32_e32 v173, v173
	v_pk_mul_f32 v[156:157], v[166:167], v[156:157]
	v_pk_mul_f32 v[160:161], v[170:171], v[160:161]
	v_pk_mul_f32 v[154:155], v[168:169], v[154:155]
	v_pk_mul_f32 v[158:159], v[172:173], v[158:159]
	v_pk_mul_f32 v[52:53], v[52:53], v[160:161]
	v_pk_mul_f32 v[50:51], v[50:51], v[156:157]
	v_pk_mul_f32 v[48:49], v[48:49], v[158:159]
	v_pk_mul_f32 v[46:47], v[46:47], v[154:155]
.LBB0_1869:
	s_nop 0
	s_and_b64 vcc, exec, s[0:1]
	s_mov_b64 s[40:41], -1
	s_waitcnt vmcnt(6)
	v_mov_b32_e32 v160, v184
	v_mov_b32_e32 v161, v185
	v_cvt_f32_ubyte1_e32 v155, v160
	v_cvt_f32_ubyte0_e32 v154, v160
	v_cvt_f32_ubyte3_e32 v159, v160
	v_cvt_f32_ubyte2_e32 v158, v160
	v_cvt_f32_ubyte1_e32 v151, v161
	v_cvt_f32_ubyte0_e32 v150, v161
	v_cvt_f32_ubyte3_e32 v157, v161
	v_cvt_f32_ubyte2_e32 v156, v161
	s_cbranch_vccnz .LBB0_1871
	v_pk_mul_f32 v[166:167], v[158:159], s[18:19] op_sel_hi:[1,0]
	v_pk_mul_f32 v[160:161], v[154:155], s[18:19] op_sel_hi:[1,0]
	v_pk_mul_f32 v[168:169], v[20:21], v[166:167]
	v_pk_mul_f32 v[166:167], v[150:151], s[18:19] op_sel_hi:[1,0]
	v_pk_mul_f32 v[170:171], v[156:157], s[18:19] op_sel_hi:[1,0]
	s_mov_b64 s[40:41], 0
	v_pk_mul_f32 v[160:161], v[18:19], v[160:161]
	v_pk_mul_f32 v[170:171], v[16:17], v[170:171]
	v_pk_mul_f32 v[172:173], v[14:15], v[166:167]
	v_cvt_pk_bf16_f32 v166, v160, v161
	v_cvt_pk_bf16_f32 v167, v168, v169
	s_nop 0
	v_cvt_pk_bf16_f32 v168, v172, v173
	v_cvt_pk_bf16_f32 v169, v170, v171
	global_store_dwordx4 v[148:149], v[166:169], off offset:256
; __device__ __forceinline__ u32x4 pack8(f32x4 v0, f32x4 v1) { u32x4 w; w.x = cvt_pk_bf16(v0[0], v0[1]); w.y = cvt_pk_bf16(v0[2], v0[3]); w.z = cvt_pk_bf16(v1[0], v1[1]); w.w = cvt_pk_bf16(v1[2], v1[3]); return w; }
; template <class T> __device__ __forceinline__ void est(T* p, T v) { if constexpr (MK_EPI_NT != 0) __builtin_nontemporal_store(v, p); else *p = v; }
;     __device__ __forceinline__ bool operator()(f32x4 (&acc)[2][2][4][2], const Unit& u, int wr, int wc, int fr, int fq) const {
;     ...
;         for (int ai = 0; ai < 2; ++ai)
; #pragma unroll
;             for (int m = 0; m < 4; ++m) { const int row = row0 + ai * 128 + m * 16;
; #pragma unroll
;                 for (int bj = 0; bj < 2; ++bj) { const int col = col0 + bj * 128; f32x4 g0, g1; unpack8_u8(*(const u32x2*)(G8 + (size_t)row * (NIN - C_G) + gc * DM + col), g0, g1);
;                     if (u.z < 2) { f32x4 h0, h1; unpack8_u8(*(const u32x2*)(G8 + (size_t)row * (NIN - C_G) + gn * DM + col), h0, h1);
; #pragma unroll
;                         for (int j = 0; j < 4; ++j) { g0[j] *= __builtin_amdgcn_rcpf(h0[j]); g1[j] *= __builtin_amdgcn_rcpf(h1[j]); }
;                         acc[ai][bj][m][0] *= g0; acc[ai][bj][m][1] *= g1;
;                     } else est((u32x4*)(mrgb + (size_t)row * DM + col), (u32x4)pack8(acc[ai][bj][m][0] * (g0 * (1.f / 255.f)), acc[ai][bj][m][1] * (g1 * (1.f / 255.f)))); } }
.LBB0_1871:
	s_andn2_b64 vcc, exec, s[40:41]
	s_cbranch_vccnz .LBB0_1873
	s_nop 0
	s_waitcnt vmcnt(3)
	v_mov_b32_e32 v148, v202
	v_mov_b32_e32 v149, v203
	v_cvt_f32_ubyte0_e32 v3, v148
	v_cvt_f32_ubyte1_e32 v147, v148
	v_cvt_f32_ubyte2_e32 v160, v148
	v_cvt_f32_ubyte3_e32 v161, v148
	v_cvt_f32_ubyte0_e32 v152, v149
	v_cvt_f32_ubyte1_e32 v153, v149
	v_cvt_f32_ubyte2_e32 v166, v149
	v_cvt_f32_ubyte3_e32 v167, v149
	v_rcp_iflag_f32_e32 v148, v3
	v_rcp_iflag_f32_e32 v152, v152
	v_rcp_iflag_f32_e32 v149, v147
	v_rcp_iflag_f32_e32 v153, v153
	v_rcp_iflag_f32_e32 v160, v160
	v_rcp_iflag_f32_e32 v161, v161
	v_rcp_iflag_f32_e32 v166, v166
	v_rcp_iflag_f32_e32 v167, v167
	v_pk_mul_f32 v[148:149], v[148:149], v[154:155]
	v_pk_mul_f32 v[154:155], v[160:161], v[158:159]
	v_pk_mul_f32 v[150:151], v[152:153], v[150:151]
	v_pk_mul_f32 v[152:153], v[166:167], v[156:157]
	v_pk_mul_f32 v[20:21], v[20:21], v[154:155]
	v_pk_mul_f32 v[18:19], v[18:19], v[148:149]
	v_pk_mul_f32 v[16:17], v[16:17], v[152:153]
	v_pk_mul_f32 v[14:15], v[14:15], v[150:151]
.LBB0_1873:
	v_add_u32_e32 v146, 0xb0, v146
	v_mov_b64_e32 v[148:149], s[64:65]
	v_mad_i64_i32 v[158:159], s[40:41], v146, s74, v[148:149]
	v_lshl_add_u64 v[148:149], v[158:159], 0, s[8:9]
	v_lshl_add_u64 v[148:149], v[148:149], 0, v[4:5]
	s_nop 0
	v_ashrrev_i32_e32 v147, 31, v146
	v_lshlrev_b64 v[146:147], 12, v[146:147]
	v_lshl_add_u64 v[146:147], s[60:61], 0, v[146:147]
	s_mov_b64 s[40:41], -1
	s_and_b64 vcc, exec, s[0:1]
	v_lshl_add_u64 v[146:147], v[4:5], 1, v[146:147]
	s_waitcnt vmcnt(4)
	v_mov_b32_e32 v160, v186
	v_mov_b32_e32 v161, v187
	v_cvt_f32_ubyte1_e32 v153, v160
	v_cvt_f32_ubyte0_e32 v152, v160
	v_cvt_f32_ubyte3_e32 v157, v160
	v_cvt_f32_ubyte2_e32 v156, v160
	v_cvt_f32_ubyte1_e32 v151, v161
	v_cvt_f32_ubyte0_e32 v150, v161
	v_cvt_f32_ubyte3_e32 v155, v161
	v_cvt_f32_ubyte2_e32 v154, v161
	s_cbranch_vccnz .LBB0_1875
	v_pk_mul_f32 v[166:167], v[156:157], s[18:19] op_sel_hi:[1,0]
	v_pk_mul_f32 v[160:161], v[152:153], s[18:19] op_sel_hi:[1,0]
	v_pk_mul_f32 v[168:169], v[44:45], v[166:167]
	v_pk_mul_f32 v[166:167], v[150:151], s[18:19] op_sel_hi:[1,0]
	v_pk_mul_f32 v[170:171], v[154:155], s[18:19] op_sel_hi:[1,0]
	s_mov_b64 s[40:41], 0
	v_pk_mul_f32 v[160:161], v[42:43], v[160:161]
	v_pk_mul_f32 v[170:171], v[40:41], v[170:171]
	v_pk_mul_f32 v[172:173], v[38:39], v[166:167]
	v_cvt_pk_bf16_f32 v166, v160, v161
	v_cvt_pk_bf16_f32 v167, v168, v169
	s_nop 0
	v_cvt_pk_bf16_f32 v168, v172, v173
	v_cvt_pk_bf16_f32 v169, v170, v171
	global_store_dwordx4 v[146:147], v[166:169], off
.LBB0_1875:
	v_lshl_add_u64 v[158:159], v[158:159], 0, s[38:39]
	s_andn2_b64 vcc, exec, s[40:41]
	v_lshl_add_u64 v[4:5], v[158:159], 0, v[4:5]
	s_cbranch_vccnz .LBB0_1877
	s_nop 0
	s_waitcnt vmcnt(1)
	v_mov_b32_e32 v158, v204
	v_mov_b32_e32 v159, v205
	v_cvt_f32_ubyte0_e32 v3, v158
	v_cvt_f32_ubyte1_e32 v161, v158
	v_cvt_f32_ubyte2_e32 v166, v158
	v_cvt_f32_ubyte3_e32 v167, v158
	v_cvt_f32_ubyte0_e32 v160, v159
	v_cvt_f32_ubyte1_e32 v168, v159
	v_cvt_f32_ubyte2_e32 v169, v159
	v_cvt_f32_ubyte3_e32 v170, v159
	v_rcp_iflag_f32_e32 v158, v3
	v_rcp_iflag_f32_e32 v160, v160
	v_rcp_iflag_f32_e32 v159, v161
	v_rcp_iflag_f32_e32 v161, v168
	v_rcp_iflag_f32_e32 v166, v166
	v_rcp_iflag_f32_e32 v167, v167
	v_rcp_iflag_f32_e32 v168, v169
	v_rcp_iflag_f32_e32 v169, v170
	v_pk_mul_f32 v[152:153], v[158:159], v[152:153]
	v_pk_mul_f32 v[156:157], v[166:167], v[156:157]
	v_pk_mul_f32 v[150:151], v[160:161], v[150:151]
	v_pk_mul_f32 v[154:155], v[168:169], v[154:155]
	v_pk_mul_f32 v[44:45], v[44:45], v[156:157]
	v_pk_mul_f32 v[42:43], v[42:43], v[152:153]
	v_pk_mul_f32 v[40:41], v[40:41], v[154:155]
	v_pk_mul_f32 v[38:39], v[38:39], v[150:151]
.LBB0_1877:
	s_nop 0
	s_and_b64 vcc, exec, s[0:1]
	s_mov_b64 s[38:39], -1
	s_waitcnt vmcnt(2)
	v_mov_b32_e32 v156, v188
	v_mov_b32_e32 v157, v189
	v_cvt_f32_ubyte1_e32 v151, v156
	v_cvt_f32_ubyte0_e32 v150, v156
	v_cvt_f32_ubyte3_e32 v155, v156
	v_cvt_f32_ubyte2_e32 v154, v156
	v_cvt_f32_ubyte1_e32 v149, v157
	v_cvt_f32_ubyte0_e32 v148, v157
	v_cvt_f32_ubyte3_e32 v153, v157
	v_cvt_f32_ubyte2_e32 v152, v157
	s_cbranch_vccz .LBB0_1880
	s_andn2_b64 vcc, exec, s[38:39]
	s_cbranch_vccz .LBB0_1881

;     __device__ __forceinline__ bool operator()(f32x4 (&acc)[2][2][4][2], const Unit& u, int wr, int wc, int fr, int fq) const {
;     ...
;                     if (u.z < 2) { f32x4 h0, h1; unpack8_u8(*(const u32x2*)(G8 + (size_t)row * (NIN - C_G) + gn * DM + col), h0, h1);
; #pragma unroll
;                         for (int j = 0; j < 4; ++j) { g0[j] *= __builtin_amdgcn_rcpf(h0[j]); g1[j] *= __builtin_amdgcn_rcpf(h1[j]); }
;                         acc[ai][bj][m][0] *= g0; acc[ai][bj][m][1] *= g1;
.LBB0_1881:
	s_nop 0
	s_waitcnt vmcnt(0)
	v_mov_b32_e32 v4, v206
	v_mov_b32_e32 v5, v207
	v_cvt_f32_ubyte0_e32 v3, v4
	v_cvt_f32_ubyte1_e32 v147, v4
	v_cvt_f32_ubyte2_e32 v156, v4
	v_cvt_f32_ubyte3_e32 v157, v4
	v_cvt_f32_ubyte0_e32 v146, v5
	v_cvt_f32_ubyte1_e32 v158, v5
	v_cvt_f32_ubyte2_e32 v159, v5
	v_cvt_f32_ubyte3_e32 v160, v5
	v_rcp_iflag_f32_e32 v4, v3
	v_rcp_iflag_f32_e32 v146, v146
	v_rcp_iflag_f32_e32 v5, v147
	v_rcp_iflag_f32_e32 v147, v158
	v_rcp_iflag_f32_e32 v156, v156
	v_rcp_iflag_f32_e32 v157, v157
	v_rcp_iflag_f32_e32 v158, v159
	v_rcp_iflag_f32_e32 v159, v160
	v_pk_mul_f32 v[4:5], v[4:5], v[150:151]
	v_pk_mul_f32 v[150:151], v[156:157], v[154:155]
	v_pk_mul_f32 v[146:147], v[146:147], v[148:149]
	v_pk_mul_f32 v[148:149], v[158:159], v[152:153]
	v_pk_mul_f32 v[12:13], v[12:13], v[150:151]
	v_pk_mul_f32 v[10:11], v[10:11], v[4:5]
	v_pk_mul_f32 v[8:9], v[8:9], v[148:149]
	v_pk_mul_f32 v[6:7], v[6:7], v[146:147]
	s_andn2_b64 vcc, exec, s[28:29]
	s_mov_b64 s[28:29], -1
	s_cbranch_vccnz .LBB0_1809
